# W-publish barrier moved behind the first gather loads of set A (both layers)
# baseline (speedup 1.0000x reference)
.Lg1_active:
	s_mov_b32 s60, 0x00ff00ff
	s_mov_b32 s61, 0x0c030c01
	v_lshrrev_b32_e32 v107, 3, v1
	v_and_b32_e32 v108, 7, v1
	v_and_b32_e32 v105, 15, v1
	v_lshrrev_b32_e32 v106, 4, v1
	s_bfe_u32 s36, s3, 0x10002
	s_lshl_b32 s58, s36, 3
	s_xor_b32 s59, s58, 8
	v_or_b32_e32 v102, s58, v107
	v_or_b32_e32 v103, s59, v107
	v_lshlrev_b32_e32 v89, 4, v108
	v_and_b32_e32 v90, 56, v1
	v_lshlrev_b32_e32 v90, 2, v90
	s_waitcnt lgkmcnt(0)
	s_lshl_b32 s58, s6, 8
	s_add_u32 s32, s16, s58
	s_addc_u32 s33, s17, 0
	s_lshl_b32 s58, s6, 10
	s_add_u32 s34, s18, s58
	s_addc_u32 s35, s19, 0
	v_lshlrev_b32_e32 v109, 4, v105
	global_load_dword v104, v109, s[32:33] offset:8
	v_lshlrev_b32_e32 v110, 4, v102
	global_load_dwordx2 v[68:69], v110, s[32:33]
	v_lshlrev_b32_e32 v111, 4, v103
	global_load_dwordx2 v[70:71], v111, s[32:33]
	v_lshlrev_b32_e32 v101, 2, v108
	v_lshl_or_b32 v110, v102, 6, v101
	global_load_dword v60, v110, s[34:35]
	global_load_dword v61, v110, s[34:35] offset:32
	v_lshl_or_b32 v111, v103, 6, v101
	global_load_dword v62, v111, s[34:35]
	global_load_dword v63, v111, s[34:35] offset:32
	global_load_dwordx4 v[2:5], v95, s[22:23]
	global_load_dwordx4 v[6:9], v98, s[22:23]
	global_load_dwordx4 v[10:13], v99, s[22:23]
	global_load_dwordx4 v[14:17], v100, s[22:23]
	v_and_b32_e32 v101, 0x7f, v0
	v_lshlrev_b32_e32 v101, 2, v101
	global_load_dword v19, v101, s[24:25]
	s_mul_i32 s48, s3, 0x1100
	s_add_u32 s48, s48, 66048
	v_mul_u32_u24_e32 v91, 0x110, v102
	v_lshl_add_u32 v91, v108, 5, v91
	v_add_u32_e32 v91, s48, v91
	v_mul_u32_u24_e32 v92, 0x110, v103
	v_lshl_add_u32 v92, v108, 5, v92
	v_add_u32_e32 v92, s48, v92
	s_waitcnt vmcnt(5)
	v_readlane_b32 s49, v69, 0
	v_readlane_b32 s50, v69, 8
	v_readlane_b32 s51, v69, 16
	v_readlane_b32 s52, v69, 24
	v_readlane_b32 s53, v69, 32
	v_readlane_b32 s54, v69, 40
	v_readlane_b32 s55, v69, 48
	v_readlane_b32 s56, v69, 56
	s_max_i32 s37, s49, s50
	s_max_i32 s37, s37, s51
	s_max_i32 s37, s37, s52
	s_max_i32 s37, s37, s53
	s_max_i32 s37, s37, s54
	s_max_i32 s37, s37, s55
	s_max_i32 s37, s37, s56
	v_readlane_b32 s49, v71, 0
	v_readlane_b32 s50, v71, 8
	v_readlane_b32 s51, v71, 16
	v_readlane_b32 s52, v71, 24
	v_readlane_b32 s53, v71, 32
	v_readlane_b32 s54, v71, 40
	v_readlane_b32 s55, v71, 48
	v_readlane_b32 s56, v71, 56
	s_max_i32 s38, s49, s50
	s_max_i32 s38, s38, s51
	s_max_i32 s38, s38, s52
	s_max_i32 s38, s38, s53
	s_max_i32 s38, s38, s54
	s_max_i32 s38, s38, s55
	s_max_i32 s38, s38, s56
	v_lshlrev_b32_e32 v103, 9, v104
	v_lshl_or_b32 v103, v106, 5, v103
	s_waitcnt vmcnt(0)
	ds_write_b128 v96, v[2:5]
	ds_write_b128 v96, v[6:9] offset:16384
	ds_write_b128 v96, v[10:13] offset:32768
	ds_write_b128 v96, v[14:17] offset:49152
	v_add_u32_e32 v101, 0x10000, v101
	ds_write_b32 v101, v19
	s_mov_b32 s39, 0

.Lg1_sel_done:
	s_min_i32 s40, s41, 32
	s_add_i32 s40, s40, 3
	s_and_b32 s40, s40, 0x3c
	s_max_i32 s40, s40, 4
	v_mov_b32_e32 v2, 0
	v_mov_b32_e32 v3, 0
	v_mov_b32_e32 v4, 0
	v_mov_b32_e32 v5, 0
	v_mov_b32_e32 v6, 0
	v_mov_b32_e32 v7, 0
	v_mov_b32_e32 v8, 0
	v_mov_b32_e32 v9, 0
	v_mov_b32_e32 v10, 0
	v_mov_b32_e32 v11, 0
	v_mov_b32_e32 v12, 0
	v_mov_b32_e32 v13, 0
	v_mov_b32_e32 v14, 0
	v_mov_b32_e32 v15, 0
	v_mov_b32_e32 v16, 0
	v_mov_b32_e32 v17, 0
	v_mov_b32_e32 v18, 0
	s_waitcnt lgkmcnt(0)
	ds_bpermute_b32 v94, v90, v73 offset:0
	ds_bpermute_b32 v95, v90, v73 offset:4
	ds_bpermute_b32 v79, v90, v73 offset:8
	s_waitcnt lgkmcnt(1)
	v_and_b32_e32 v84, 0xffff, v94
	v_lshl_or_b32 v83, v84, 7, v89
	v_cmp_lt_i32_e32 vcc, 0, v78
	s_mov_b64 exec, vcc
	global_load_dwordx4 v[20:23], v83, s[12:13]
	s_mov_b64 exec, -1
	v_lshlrev_b32_e32 v109, 1, v84
	global_load_ushort v52, v109, s[14:15]
	v_lshrrev_b32_e32 v84, 16, v94
	v_lshl_or_b32 v83, v84, 7, v89
	v_cmp_lt_i32_e32 vcc, 1, v78
	s_mov_b64 exec, vcc
	global_load_dwordx4 v[24:27], v83, s[12:13]
	s_mov_b64 exec, -1
	v_lshlrev_b32_e32 v109, 1, v84
	global_load_ushort v53, v109, s[14:15]
	v_and_b32_e32 v84, 0xffff, v95
	v_lshl_or_b32 v83, v84, 7, v89
	v_cmp_lt_i32_e32 vcc, 2, v78
	s_mov_b64 exec, vcc
	global_load_dwordx4 v[28:31], v83, s[12:13]
	s_mov_b64 exec, -1
	v_lshlrev_b32_e32 v109, 1, v84
	global_load_ushort v54, v109, s[14:15]
	v_lshrrev_b32_e32 v84, 16, v95
	v_lshl_or_b32 v83, v84, 7, v89
	v_cmp_lt_i32_e32 vcc, 3, v78
	s_mov_b64 exec, vcc
	global_load_dwordx4 v[32:35], v83, s[12:13]
	s_mov_b64 exec, -1
	v_lshlrev_b32_e32 v109, 1, v84
	global_load_ushort v55, v109, s[14:15]
	s_cmp_eq_u32 s39, 0
	s_cbranch_scc0 .Lg1_nobar
	s_waitcnt lgkmcnt(0)
	s_barrier
.Lg1_nobar:
	s_cmp_le_u32 s40, 4
	s_cbranch_scc1 .Lg1_tail0
	s_waitcnt lgkmcnt(0)
	ds_bpermute_b32 v80, v90, v73 offset:12
	s_waitcnt vmcnt(6)
	v_cvt_f32_f16_e32 v52, v52
	v_cvt_f32_ubyte0_e32 v85, v20
	v_cvt_f32_ubyte1_e32 v86, v20
	v_cvt_f32_ubyte2_e32 v87, v20
	v_cvt_f32_ubyte3_e32 v88, v20
	v_fmac_f32_e32 v2, v85, v52
	v_fmac_f32_e32 v3, v86, v52
	v_fmac_f32_e32 v4, v87, v52
	v_fmac_f32_e32 v5, v88, v52
	v_cvt_f32_ubyte0_e32 v85, v21
	v_cvt_f32_ubyte1_e32 v86, v21
	v_cvt_f32_ubyte2_e32 v87, v21
	v_cvt_f32_ubyte3_e32 v88, v21
	v_fmac_f32_e32 v6, v85, v52
	v_fmac_f32_e32 v7, v86, v52
	v_fmac_f32_e32 v8, v87, v52
	v_fmac_f32_e32 v9, v88, v52
	v_cvt_f32_ubyte0_e32 v85, v22
	v_cvt_f32_ubyte1_e32 v86, v22
	v_cvt_f32_ubyte2_e32 v87, v22
	v_cvt_f32_ubyte3_e32 v88, v22
	v_fmac_f32_e32 v10, v85, v52
	v_fmac_f32_e32 v11, v86, v52
	v_fmac_f32_e32 v12, v87, v52
	v_fmac_f32_e32 v13, v88, v52
	v_cvt_f32_ubyte0_e32 v85, v23
	v_cvt_f32_ubyte1_e32 v86, v23
	v_cvt_f32_ubyte2_e32 v87, v23
	v_cvt_f32_ubyte3_e32 v88, v23
	v_fmac_f32_e32 v14, v85, v52
	v_fmac_f32_e32 v15, v86, v52
	v_fmac_f32_e32 v16, v87, v52
	v_fmac_f32_e32 v17, v88, v52
	v_add_f32_e32 v18, v18, v52
	v_and_b32_e32 v84, 0xffff, v79
	v_lshl_or_b32 v83, v84, 7, v89
	v_cmp_lt_i32_e32 vcc, 4, v78
	s_mov_b64 exec, vcc
	global_load_dwordx4 v[20:23], v83, s[12:13]
	s_mov_b64 exec, -1
	v_lshlrev_b32_e32 v109, 1, v84
	global_load_ushort v52, v109, s[14:15]
	s_waitcnt vmcnt(6)
	v_cvt_f32_f16_e32 v53, v53
	v_cvt_f32_ubyte0_e32 v85, v24
	v_cvt_f32_ubyte1_e32 v86, v24
	v_cvt_f32_ubyte2_e32 v87, v24
	v_cvt_f32_ubyte3_e32 v88, v24
	v_fmac_f32_e32 v2, v85, v53
	v_fmac_f32_e32 v3, v86, v53
	v_fmac_f32_e32 v4, v87, v53
	v_fmac_f32_e32 v5, v88, v53
	v_cvt_f32_ubyte0_e32 v85, v25
	v_cvt_f32_ubyte1_e32 v86, v25
	v_cvt_f32_ubyte2_e32 v87, v25
	v_cvt_f32_ubyte3_e32 v88, v25
	v_fmac_f32_e32 v6, v85, v53
	v_fmac_f32_e32 v7, v86, v53
	v_fmac_f32_e32 v8, v87, v53
	v_fmac_f32_e32 v9, v88, v53
	v_cvt_f32_ubyte0_e32 v85, v26
	v_cvt_f32_ubyte1_e32 v86, v26
	v_cvt_f32_ubyte2_e32 v87, v26
	v_cvt_f32_ubyte3_e32 v88, v26
	v_fmac_f32_e32 v10, v85, v53
	v_fmac_f32_e32 v11, v86, v53
	v_fmac_f32_e32 v12, v87, v53
	v_fmac_f32_e32 v13, v88, v53
	v_cvt_f32_ubyte0_e32 v85, v27
	v_cvt_f32_ubyte1_e32 v86, v27
	v_cvt_f32_ubyte2_e32 v87, v27
	v_cvt_f32_ubyte3_e32 v88, v27
	v_fmac_f32_e32 v14, v85, v53
	v_fmac_f32_e32 v15, v86, v53
	v_fmac_f32_e32 v16, v87, v53
	v_fmac_f32_e32 v17, v88, v53
	v_add_f32_e32 v18, v18, v53
	v_lshrrev_b32_e32 v84, 16, v79
	v_lshl_or_b32 v83, v84, 7, v89
	v_cmp_lt_i32_e32 vcc, 5, v78
	s_mov_b64 exec, vcc
	global_load_dwordx4 v[24:27], v83, s[12:13]
	s_mov_b64 exec, -1
	v_lshlrev_b32_e32 v109, 1, v84
	global_load_ushort v53, v109, s[14:15]
	s_waitcnt lgkmcnt(0)
	ds_bpermute_b32 v79, v90, v73 offset:16
	s_waitcnt vmcnt(6)
	v_cvt_f32_f16_e32 v54, v54
	v_cvt_f32_ubyte0_e32 v85, v28
	v_cvt_f32_ubyte1_e32 v86, v28
	v_cvt_f32_ubyte2_e32 v87, v28
	v_cvt_f32_ubyte3_e32 v88, v28
	v_fmac_f32_e32 v2, v85, v54
	v_fmac_f32_e32 v3, v86, v54
	v_fmac_f32_e32 v4, v87, v54
	v_fmac_f32_e32 v5, v88, v54
	v_cvt_f32_ubyte0_e32 v85, v29
	v_cvt_f32_ubyte1_e32 v86, v29
	v_cvt_f32_ubyte2_e32 v87, v29
	v_cvt_f32_ubyte3_e32 v88, v29
	v_fmac_f32_e32 v6, v85, v54
	v_fmac_f32_e32 v7, v86, v54
	v_fmac_f32_e32 v8, v87, v54
	v_fmac_f32_e32 v9, v88, v54
	v_cvt_f32_ubyte0_e32 v85, v30
	v_cvt_f32_ubyte1_e32 v86, v30
	v_cvt_f32_ubyte2_e32 v87, v30
	v_cvt_f32_ubyte3_e32 v88, v30
	v_fmac_f32_e32 v10, v85, v54
	v_fmac_f32_e32 v11, v86, v54
	v_fmac_f32_e32 v12, v87, v54
	v_fmac_f32_e32 v13, v88, v54
	v_cvt_f32_ubyte0_e32 v85, v31
	v_cvt_f32_ubyte1_e32 v86, v31
	v_cvt_f32_ubyte2_e32 v87, v31
	v_cvt_f32_ubyte3_e32 v88, v31
	v_fmac_f32_e32 v14, v85, v54
	v_fmac_f32_e32 v15, v86, v54
	v_fmac_f32_e32 v16, v87, v54
	v_fmac_f32_e32 v17, v88, v54
	v_add_f32_e32 v18, v18, v54
	v_and_b32_e32 v84, 0xffff, v80
	v_lshl_or_b32 v83, v84, 7, v89
	v_cmp_lt_i32_e32 vcc, 6, v78
	s_mov_b64 exec, vcc
	global_load_dwordx4 v[28:31], v83, s[12:13]
	s_mov_b64 exec, -1
	v_lshlrev_b32_e32 v109, 1, v84
	global_load_ushort v54, v109, s[14:15]
	s_waitcnt vmcnt(6)
	v_cvt_f32_f16_e32 v55, v55
	v_cvt_f32_ubyte0_e32 v85, v32
	v_cvt_f32_ubyte1_e32 v86, v32
	v_cvt_f32_ubyte2_e32 v87, v32
	v_cvt_f32_ubyte3_e32 v88, v32
	v_fmac_f32_e32 v2, v85, v55
	v_fmac_f32_e32 v3, v86, v55
	v_fmac_f32_e32 v4, v87, v55
	v_fmac_f32_e32 v5, v88, v55
	v_cvt_f32_ubyte0_e32 v85, v33
	v_cvt_f32_ubyte1_e32 v86, v33
	v_cvt_f32_ubyte2_e32 v87, v33
	v_cvt_f32_ubyte3_e32 v88, v33
	v_fmac_f32_e32 v6, v85, v55
	v_fmac_f32_e32 v7, v86, v55
	v_fmac_f32_e32 v8, v87, v55
	v_fmac_f32_e32 v9, v88, v55
	v_cvt_f32_ubyte0_e32 v85, v34
	v_cvt_f32_ubyte1_e32 v86, v34
	v_cvt_f32_ubyte2_e32 v87, v34
	v_cvt_f32_ubyte3_e32 v88, v34
	v_fmac_f32_e32 v10, v85, v55
	v_fmac_f32_e32 v11, v86, v55
	v_fmac_f32_e32 v12, v87, v55
	v_fmac_f32_e32 v13, v88, v55
	v_cvt_f32_ubyte0_e32 v85, v35
	v_cvt_f32_ubyte1_e32 v86, v35
	v_cvt_f32_ubyte2_e32 v87, v35
	v_cvt_f32_ubyte3_e32 v88, v35
	v_fmac_f32_e32 v14, v85, v55
	v_fmac_f32_e32 v15, v86, v55
	v_fmac_f32_e32 v16, v87, v55
	v_fmac_f32_e32 v17, v88, v55
	v_add_f32_e32 v18, v18, v55
	v_lshrrev_b32_e32 v84, 16, v80
	v_lshl_or_b32 v83, v84, 7, v89
	v_cmp_lt_i32_e32 vcc, 7, v78
	s_mov_b64 exec, vcc
	global_load_dwordx4 v[32:35], v83, s[12:13]
	s_mov_b64 exec, -1
	v_lshlrev_b32_e32 v109, 1, v84
	global_load_ushort v55, v109, s[14:15]
	s_cmp_le_u32 s40, 8
	s_cbranch_scc1 .Lg1_tail0
	s_waitcnt lgkmcnt(0)
	ds_bpermute_b32 v80, v90, v73 offset:20
	s_waitcnt vmcnt(6)
	v_cvt_f32_f16_e32 v52, v52
	v_cvt_f32_ubyte0_e32 v85, v20
	v_cvt_f32_ubyte1_e32 v86, v20
	v_cvt_f32_ubyte2_e32 v87, v20
	v_cvt_f32_ubyte3_e32 v88, v20
	v_fmac_f32_e32 v2, v85, v52
	v_fmac_f32_e32 v3, v86, v52
	v_fmac_f32_e32 v4, v87, v52
	v_fmac_f32_e32 v5, v88, v52
	v_cvt_f32_ubyte0_e32 v85, v21
	v_cvt_f32_ubyte1_e32 v86, v21
	v_cvt_f32_ubyte2_e32 v87, v21
	v_cvt_f32_ubyte3_e32 v88, v21
	v_fmac_f32_e32 v6, v85, v52
	v_fmac_f32_e32 v7, v86, v52
	v_fmac_f32_e32 v8, v87, v52
	v_fmac_f32_e32 v9, v88, v52
	v_cvt_f32_ubyte0_e32 v85, v22
	v_cvt_f32_ubyte1_e32 v86, v22
	v_cvt_f32_ubyte2_e32 v87, v22
	v_cvt_f32_ubyte3_e32 v88, v22
	v_fmac_f32_e32 v10, v85, v52
	v_fmac_f32_e32 v11, v86, v52
	v_fmac_f32_e32 v12, v87, v52
	v_fmac_f32_e32 v13, v88, v52
	v_cvt_f32_ubyte0_e32 v85, v23
	v_cvt_f32_ubyte1_e32 v86, v23
	v_cvt_f32_ubyte2_e32 v87, v23
	v_cvt_f32_ubyte3_e32 v88, v23
	v_fmac_f32_e32 v14, v85, v52
	v_fmac_f32_e32 v15, v86, v52
	v_fmac_f32_e32 v16, v87, v52
	v_fmac_f32_e32 v17, v88, v52
	v_add_f32_e32 v18, v18, v52
	v_and_b32_e32 v84, 0xffff, v79
	v_lshl_or_b32 v83, v84, 7, v89
	v_cmp_lt_i32_e32 vcc, 8, v78
	s_mov_b64 exec, vcc
	global_load_dwordx4 v[20:23], v83, s[12:13]
	s_mov_b64 exec, -1
	v_lshlrev_b32_e32 v109, 1, v84
	global_load_ushort v52, v109, s[14:15]
	s_waitcnt vmcnt(6)
	v_cvt_f32_f16_e32 v53, v53
	v_cvt_f32_ubyte0_e32 v85, v24
	v_cvt_f32_ubyte1_e32 v86, v24
	v_cvt_f32_ubyte2_e32 v87, v24
	v_cvt_f32_ubyte3_e32 v88, v24
	v_fmac_f32_e32 v2, v85, v53
	v_fmac_f32_e32 v3, v86, v53
	v_fmac_f32_e32 v4, v87, v53
	v_fmac_f32_e32 v5, v88, v53
	v_cvt_f32_ubyte0_e32 v85, v25
	v_cvt_f32_ubyte1_e32 v86, v25
	v_cvt_f32_ubyte2_e32 v87, v25
	v_cvt_f32_ubyte3_e32 v88, v25
	v_fmac_f32_e32 v6, v85, v53
	v_fmac_f32_e32 v7, v86, v53
	v_fmac_f32_e32 v8, v87, v53
	v_fmac_f32_e32 v9, v88, v53
	v_cvt_f32_ubyte0_e32 v85, v26
	v_cvt_f32_ubyte1_e32 v86, v26
	v_cvt_f32_ubyte2_e32 v87, v26
	v_cvt_f32_ubyte3_e32 v88, v26
	v_fmac_f32_e32 v10, v85, v53
	v_fmac_f32_e32 v11, v86, v53
	v_fmac_f32_e32 v12, v87, v53
	v_fmac_f32_e32 v13, v88, v53
	v_cvt_f32_ubyte0_e32 v85, v27
	v_cvt_f32_ubyte1_e32 v86, v27
	v_cvt_f32_ubyte2_e32 v87, v27
	v_cvt_f32_ubyte3_e32 v88, v27
	v_fmac_f32_e32 v14, v85, v53
	v_fmac_f32_e32 v15, v86, v53
	v_fmac_f32_e32 v16, v87, v53
	v_fmac_f32_e32 v17, v88, v53
	v_add_f32_e32 v18, v18, v53
	v_lshrrev_b32_e32 v84, 16, v79
	v_lshl_or_b32 v83, v84, 7, v89
	v_cmp_lt_i32_e32 vcc, 9, v78
	s_mov_b64 exec, vcc
	global_load_dwordx4 v[24:27], v83, s[12:13]
	s_mov_b64 exec, -1
	v_lshlrev_b32_e32 v109, 1, v84
	global_load_ushort v53, v109, s[14:15]
	s_waitcnt lgkmcnt(0)
	ds_bpermute_b32 v79, v90, v73 offset:24
	s_waitcnt vmcnt(6)
	v_cvt_f32_f16_e32 v54, v54
	v_cvt_f32_ubyte0_e32 v85, v28
	v_cvt_f32_ubyte1_e32 v86, v28
	v_cvt_f32_ubyte2_e32 v87, v28
	v_cvt_f32_ubyte3_e32 v88, v28
	v_fmac_f32_e32 v2, v85, v54
	v_fmac_f32_e32 v3, v86, v54
	v_fmac_f32_e32 v4, v87, v54
	v_fmac_f32_e32 v5, v88, v54
	v_cvt_f32_ubyte0_e32 v85, v29
	v_cvt_f32_ubyte1_e32 v86, v29
	v_cvt_f32_ubyte2_e32 v87, v29
	v_cvt_f32_ubyte3_e32 v88, v29
	v_fmac_f32_e32 v6, v85, v54
	v_fmac_f32_e32 v7, v86, v54
	v_fmac_f32_e32 v8, v87, v54
	v_fmac_f32_e32 v9, v88, v54
	v_cvt_f32_ubyte0_e32 v85, v30
	v_cvt_f32_ubyte1_e32 v86, v30
	v_cvt_f32_ubyte2_e32 v87, v30
	v_cvt_f32_ubyte3_e32 v88, v30
	v_fmac_f32_e32 v10, v85, v54
	v_fmac_f32_e32 v11, v86, v54
	v_fmac_f32_e32 v12, v87, v54
	v_fmac_f32_e32 v13, v88, v54
	v_cvt_f32_ubyte0_e32 v85, v31
	v_cvt_f32_ubyte1_e32 v86, v31
	v_cvt_f32_ubyte2_e32 v87, v31
	v_cvt_f32_ubyte3_e32 v88, v31
	v_fmac_f32_e32 v14, v85, v54
	v_fmac_f32_e32 v15, v86, v54
	v_fmac_f32_e32 v16, v87, v54
	v_fmac_f32_e32 v17, v88, v54
	v_add_f32_e32 v18, v18, v54
	v_and_b32_e32 v84, 0xffff, v80
	v_lshl_or_b32 v83, v84, 7, v89
	v_cmp_lt_i32_e32 vcc, 10, v78
	s_mov_b64 exec, vcc
	global_load_dwordx4 v[28:31], v83, s[12:13]
	s_mov_b64 exec, -1
	v_lshlrev_b32_e32 v109, 1, v84
	global_load_ushort v54, v109, s[14:15]
	s_waitcnt vmcnt(6)
	v_cvt_f32_f16_e32 v55, v55
	v_cvt_f32_ubyte0_e32 v85, v32
	v_cvt_f32_ubyte1_e32 v86, v32
	v_cvt_f32_ubyte2_e32 v87, v32
	v_cvt_f32_ubyte3_e32 v88, v32
	v_fmac_f32_e32 v2, v85, v55
	v_fmac_f32_e32 v3, v86, v55
	v_fmac_f32_e32 v4, v87, v55
	v_fmac_f32_e32 v5, v88, v55
	v_cvt_f32_ubyte0_e32 v85, v33
	v_cvt_f32_ubyte1_e32 v86, v33
	v_cvt_f32_ubyte2_e32 v87, v33
	v_cvt_f32_ubyte3_e32 v88, v33
	v_fmac_f32_e32 v6, v85, v55
	v_fmac_f32_e32 v7, v86, v55
	v_fmac_f32_e32 v8, v87, v55
	v_fmac_f32_e32 v9, v88, v55
	v_cvt_f32_ubyte0_e32 v85, v34
	v_cvt_f32_ubyte1_e32 v86, v34
	v_cvt_f32_ubyte2_e32 v87, v34
	v_cvt_f32_ubyte3_e32 v88, v34
	v_fmac_f32_e32 v10, v85, v55
	v_fmac_f32_e32 v11, v86, v55
	v_fmac_f32_e32 v12, v87, v55
	v_fmac_f32_e32 v13, v88, v55
	v_cvt_f32_ubyte0_e32 v85, v35
	v_cvt_f32_ubyte1_e32 v86, v35
	v_cvt_f32_ubyte2_e32 v87, v35
	v_cvt_f32_ubyte3_e32 v88, v35
	v_fmac_f32_e32 v14, v85, v55
	v_fmac_f32_e32 v15, v86, v55
	v_fmac_f32_e32 v16, v87, v55
	v_fmac_f32_e32 v17, v88, v55
	v_add_f32_e32 v18, v18, v55
	v_lshrrev_b32_e32 v84, 16, v80
	v_lshl_or_b32 v83, v84, 7, v89
	v_cmp_lt_i32_e32 vcc, 11, v78
	s_mov_b64 exec, vcc
	global_load_dwordx4 v[32:35], v83, s[12:13]
	s_mov_b64 exec, -1
	v_lshlrev_b32_e32 v109, 1, v84
	global_load_ushort v55, v109, s[14:15]
	s_cmp_le_u32 s40, 12
	s_cbranch_scc1 .Lg1_tail0
	s_waitcnt lgkmcnt(0)
	ds_bpermute_b32 v80, v90, v73 offset:28
	s_waitcnt vmcnt(6)
	v_cvt_f32_f16_e32 v52, v52
	v_cvt_f32_ubyte0_e32 v85, v20
	v_cvt_f32_ubyte1_e32 v86, v20
	v_cvt_f32_ubyte2_e32 v87, v20
	v_cvt_f32_ubyte3_e32 v88, v20
	v_fmac_f32_e32 v2, v85, v52
	v_fmac_f32_e32 v3, v86, v52
	v_fmac_f32_e32 v4, v87, v52
	v_fmac_f32_e32 v5, v88, v52
	v_cvt_f32_ubyte0_e32 v85, v21
	v_cvt_f32_ubyte1_e32 v86, v21
	v_cvt_f32_ubyte2_e32 v87, v21
	v_cvt_f32_ubyte3_e32 v88, v21
	v_fmac_f32_e32 v6, v85, v52
	v_fmac_f32_e32 v7, v86, v52
	v_fmac_f32_e32 v8, v87, v52
	v_fmac_f32_e32 v9, v88, v52
	v_cvt_f32_ubyte0_e32 v85, v22
	v_cvt_f32_ubyte1_e32 v86, v22
	v_cvt_f32_ubyte2_e32 v87, v22
	v_cvt_f32_ubyte3_e32 v88, v22
	v_fmac_f32_e32 v10, v85, v52
	v_fmac_f32_e32 v11, v86, v52
	v_fmac_f32_e32 v12, v87, v52
	v_fmac_f32_e32 v13, v88, v52
	v_cvt_f32_ubyte0_e32 v85, v23
	v_cvt_f32_ubyte1_e32 v86, v23
	v_cvt_f32_ubyte2_e32 v87, v23
	v_cvt_f32_ubyte3_e32 v88, v23
	v_fmac_f32_e32 v14, v85, v52
	v_fmac_f32_e32 v15, v86, v52
	v_fmac_f32_e32 v16, v87, v52
	v_fmac_f32_e32 v17, v88, v52
	v_add_f32_e32 v18, v18, v52
	v_and_b32_e32 v84, 0xffff, v79
	v_lshl_or_b32 v83, v84, 7, v89
	v_cmp_lt_i32_e32 vcc, 12, v78
	s_mov_b64 exec, vcc
	global_load_dwordx4 v[20:23], v83, s[12:13]
	s_mov_b64 exec, -1
	v_lshlrev_b32_e32 v109, 1, v84
	global_load_ushort v52, v109, s[14:15]
	s_waitcnt vmcnt(6)
	v_cvt_f32_f16_e32 v53, v53
	v_cvt_f32_ubyte0_e32 v85, v24
	v_cvt_f32_ubyte1_e32 v86, v24
	v_cvt_f32_ubyte2_e32 v87, v24
	v_cvt_f32_ubyte3_e32 v88, v24
	v_fmac_f32_e32 v2, v85, v53
	v_fmac_f32_e32 v3, v86, v53
	v_fmac_f32_e32 v4, v87, v53
	v_fmac_f32_e32 v5, v88, v53
	v_cvt_f32_ubyte0_e32 v85, v25
	v_cvt_f32_ubyte1_e32 v86, v25
	v_cvt_f32_ubyte2_e32 v87, v25
	v_cvt_f32_ubyte3_e32 v88, v25
	v_fmac_f32_e32 v6, v85, v53
	v_fmac_f32_e32 v7, v86, v53
	v_fmac_f32_e32 v8, v87, v53
	v_fmac_f32_e32 v9, v88, v53
	v_cvt_f32_ubyte0_e32 v85, v26
	v_cvt_f32_ubyte1_e32 v86, v26
	v_cvt_f32_ubyte2_e32 v87, v26
	v_cvt_f32_ubyte3_e32 v88, v26
	v_fmac_f32_e32 v10, v85, v53
	v_fmac_f32_e32 v11, v86, v53
	v_fmac_f32_e32 v12, v87, v53
	v_fmac_f32_e32 v13, v88, v53
	v_cvt_f32_ubyte0_e32 v85, v27
	v_cvt_f32_ubyte1_e32 v86, v27
	v_cvt_f32_ubyte2_e32 v87, v27
	v_cvt_f32_ubyte3_e32 v88, v27
	v_fmac_f32_e32 v14, v85, v53
	v_fmac_f32_e32 v15, v86, v53
	v_fmac_f32_e32 v16, v87, v53
	v_fmac_f32_e32 v17, v88, v53
	v_add_f32_e32 v18, v18, v53
	v_lshrrev_b32_e32 v84, 16, v79
	v_lshl_or_b32 v83, v84, 7, v89
	v_cmp_lt_i32_e32 vcc, 13, v78
	s_mov_b64 exec, vcc
	global_load_dwordx4 v[24:27], v83, s[12:13]
	s_mov_b64 exec, -1
	v_lshlrev_b32_e32 v109, 1, v84
	global_load_ushort v53, v109, s[14:15]
	s_waitcnt lgkmcnt(0)
	ds_bpermute_b32 v79, v90, v74 offset:0
	s_waitcnt vmcnt(6)
	v_cvt_f32_f16_e32 v54, v54
	v_cvt_f32_ubyte0_e32 v85, v28
	v_cvt_f32_ubyte1_e32 v86, v28
	v_cvt_f32_ubyte2_e32 v87, v28
	v_cvt_f32_ubyte3_e32 v88, v28
	v_fmac_f32_e32 v2, v85, v54
	v_fmac_f32_e32 v3, v86, v54
	v_fmac_f32_e32 v4, v87, v54
	v_fmac_f32_e32 v5, v88, v54
	v_cvt_f32_ubyte0_e32 v85, v29
	v_cvt_f32_ubyte1_e32 v86, v29
	v_cvt_f32_ubyte2_e32 v87, v29
	v_cvt_f32_ubyte3_e32 v88, v29
	v_fmac_f32_e32 v6, v85, v54
	v_fmac_f32_e32 v7, v86, v54
	v_fmac_f32_e32 v8, v87, v54
	v_fmac_f32_e32 v9, v88, v54
	v_cvt_f32_ubyte0_e32 v85, v30
	v_cvt_f32_ubyte1_e32 v86, v30
	v_cvt_f32_ubyte2_e32 v87, v30
	v_cvt_f32_ubyte3_e32 v88, v30
	v_fmac_f32_e32 v10, v85, v54
	v_fmac_f32_e32 v11, v86, v54
	v_fmac_f32_e32 v12, v87, v54
	v_fmac_f32_e32 v13, v88, v54
	v_cvt_f32_ubyte0_e32 v85, v31
	v_cvt_f32_ubyte1_e32 v86, v31
	v_cvt_f32_ubyte2_e32 v87, v31
	v_cvt_f32_ubyte3_e32 v88, v31
	v_fmac_f32_e32 v14, v85, v54
	v_fmac_f32_e32 v15, v86, v54
	v_fmac_f32_e32 v16, v87, v54
	v_fmac_f32_e32 v17, v88, v54
	v_add_f32_e32 v18, v18, v54
	v_and_b32_e32 v84, 0xffff, v80
	v_lshl_or_b32 v83, v84, 7, v89
	v_cmp_lt_i32_e32 vcc, 14, v78
	s_mov_b64 exec, vcc
	global_load_dwordx4 v[28:31], v83, s[12:13]
	s_mov_b64 exec, -1
	v_lshlrev_b32_e32 v109, 1, v84
	global_load_ushort v54, v109, s[14:15]
	s_waitcnt vmcnt(6)
	v_cvt_f32_f16_e32 v55, v55
	v_cvt_f32_ubyte0_e32 v85, v32
	v_cvt_f32_ubyte1_e32 v86, v32
	v_cvt_f32_ubyte2_e32 v87, v32
	v_cvt_f32_ubyte3_e32 v88, v32
	v_fmac_f32_e32 v2, v85, v55
	v_fmac_f32_e32 v3, v86, v55
	v_fmac_f32_e32 v4, v87, v55
	v_fmac_f32_e32 v5, v88, v55
	v_cvt_f32_ubyte0_e32 v85, v33
	v_cvt_f32_ubyte1_e32 v86, v33
	v_cvt_f32_ubyte2_e32 v87, v33
	v_cvt_f32_ubyte3_e32 v88, v33
	v_fmac_f32_e32 v6, v85, v55
	v_fmac_f32_e32 v7, v86, v55
	v_fmac_f32_e32 v8, v87, v55
	v_fmac_f32_e32 v9, v88, v55
	v_cvt_f32_ubyte0_e32 v85, v34
	v_cvt_f32_ubyte1_e32 v86, v34
	v_cvt_f32_ubyte2_e32 v87, v34
	v_cvt_f32_ubyte3_e32 v88, v34
	v_fmac_f32_e32 v10, v85, v55
	v_fmac_f32_e32 v11, v86, v55
	v_fmac_f32_e32 v12, v87, v55
	v_fmac_f32_e32 v13, v88, v55
	v_cvt_f32_ubyte0_e32 v85, v35
	v_cvt_f32_ubyte1_e32 v86, v35
	v_cvt_f32_ubyte2_e32 v87, v35
	v_cvt_f32_ubyte3_e32 v88, v35
	v_fmac_f32_e32 v14, v85, v55
	v_fmac_f32_e32 v15, v86, v55
	v_fmac_f32_e32 v16, v87, v55
	v_fmac_f32_e32 v17, v88, v55
	v_add_f32_e32 v18, v18, v55
	v_lshrrev_b32_e32 v84, 16, v80
	v_lshl_or_b32 v83, v84, 7, v89
	v_cmp_lt_i32_e32 vcc, 15, v78
	s_mov_b64 exec, vcc
	global_load_dwordx4 v[32:35], v83, s[12:13]
	s_mov_b64 exec, -1
	v_lshlrev_b32_e32 v109, 1, v84
	global_load_ushort v55, v109, s[14:15]
	s_cmp_le_u32 s40, 16
	s_cbranch_scc1 .Lg1_tail0
	s_waitcnt lgkmcnt(0)
	ds_bpermute_b32 v80, v90, v74 offset:4
	s_waitcnt vmcnt(6)
	v_cvt_f32_f16_e32 v52, v52
	v_cvt_f32_ubyte0_e32 v85, v20
	v_cvt_f32_ubyte1_e32 v86, v20
	v_cvt_f32_ubyte2_e32 v87, v20
	v_cvt_f32_ubyte3_e32 v88, v20
	v_fmac_f32_e32 v2, v85, v52
	v_fmac_f32_e32 v3, v86, v52
	v_fmac_f32_e32 v4, v87, v52
	v_fmac_f32_e32 v5, v88, v52
	v_cvt_f32_ubyte0_e32 v85, v21
	v_cvt_f32_ubyte1_e32 v86, v21
	v_cvt_f32_ubyte2_e32 v87, v21
	v_cvt_f32_ubyte3_e32 v88, v21
	v_fmac_f32_e32 v6, v85, v52
	v_fmac_f32_e32 v7, v86, v52
	v_fmac_f32_e32 v8, v87, v52
	v_fmac_f32_e32 v9, v88, v52
	v_cvt_f32_ubyte0_e32 v85, v22
	v_cvt_f32_ubyte1_e32 v86, v22
	v_cvt_f32_ubyte2_e32 v87, v22
	v_cvt_f32_ubyte3_e32 v88, v22
	v_fmac_f32_e32 v10, v85, v52
	v_fmac_f32_e32 v11, v86, v52
	v_fmac_f32_e32 v12, v87, v52
	v_fmac_f32_e32 v13, v88, v52
	v_cvt_f32_ubyte0_e32 v85, v23
	v_cvt_f32_ubyte1_e32 v86, v23
	v_cvt_f32_ubyte2_e32 v87, v23
	v_cvt_f32_ubyte3_e32 v88, v23
	v_fmac_f32_e32 v14, v85, v52
	v_fmac_f32_e32 v15, v86, v52
	v_fmac_f32_e32 v16, v87, v52
	v_fmac_f32_e32 v17, v88, v52
	v_add_f32_e32 v18, v18, v52
	v_and_b32_e32 v84, 0xffff, v79
	v_lshl_or_b32 v83, v84, 7, v89
	v_cmp_lt_i32_e32 vcc, 16, v78
	s_mov_b64 exec, vcc
	global_load_dwordx4 v[20:23], v83, s[12:13]
	s_mov_b64 exec, -1
	v_lshlrev_b32_e32 v109, 1, v84
	global_load_ushort v52, v109, s[14:15]
	s_waitcnt vmcnt(6)
	v_cvt_f32_f16_e32 v53, v53
	v_cvt_f32_ubyte0_e32 v85, v24
	v_cvt_f32_ubyte1_e32 v86, v24
	v_cvt_f32_ubyte2_e32 v87, v24
	v_cvt_f32_ubyte3_e32 v88, v24
	v_fmac_f32_e32 v2, v85, v53
	v_fmac_f32_e32 v3, v86, v53
	v_fmac_f32_e32 v4, v87, v53
	v_fmac_f32_e32 v5, v88, v53
	v_cvt_f32_ubyte0_e32 v85, v25
	v_cvt_f32_ubyte1_e32 v86, v25
	v_cvt_f32_ubyte2_e32 v87, v25
	v_cvt_f32_ubyte3_e32 v88, v25
	v_fmac_f32_e32 v6, v85, v53
	v_fmac_f32_e32 v7, v86, v53
	v_fmac_f32_e32 v8, v87, v53
	v_fmac_f32_e32 v9, v88, v53
	v_cvt_f32_ubyte0_e32 v85, v26
	v_cvt_f32_ubyte1_e32 v86, v26
	v_cvt_f32_ubyte2_e32 v87, v26
	v_cvt_f32_ubyte3_e32 v88, v26
	v_fmac_f32_e32 v10, v85, v53
	v_fmac_f32_e32 v11, v86, v53
	v_fmac_f32_e32 v12, v87, v53
	v_fmac_f32_e32 v13, v88, v53
	v_cvt_f32_ubyte0_e32 v85, v27
	v_cvt_f32_ubyte1_e32 v86, v27
	v_cvt_f32_ubyte2_e32 v87, v27
	v_cvt_f32_ubyte3_e32 v88, v27
	v_fmac_f32_e32 v14, v85, v53
	v_fmac_f32_e32 v15, v86, v53
	v_fmac_f32_e32 v16, v87, v53
	v_fmac_f32_e32 v17, v88, v53
	v_add_f32_e32 v18, v18, v53
	v_lshrrev_b32_e32 v84, 16, v79
	v_lshl_or_b32 v83, v84, 7, v89
	v_cmp_lt_i32_e32 vcc, 17, v78
	s_mov_b64 exec, vcc
	global_load_dwordx4 v[24:27], v83, s[12:13]
	s_mov_b64 exec, -1
	v_lshlrev_b32_e32 v109, 1, v84
	global_load_ushort v53, v109, s[14:15]
	s_waitcnt lgkmcnt(0)
	ds_bpermute_b32 v79, v90, v74 offset:8
	s_waitcnt vmcnt(6)
	v_cvt_f32_f16_e32 v54, v54
	v_cvt_f32_ubyte0_e32 v85, v28
	v_cvt_f32_ubyte1_e32 v86, v28
	v_cvt_f32_ubyte2_e32 v87, v28
	v_cvt_f32_ubyte3_e32 v88, v28
	v_fmac_f32_e32 v2, v85, v54
	v_fmac_f32_e32 v3, v86, v54
	v_fmac_f32_e32 v4, v87, v54
	v_fmac_f32_e32 v5, v88, v54
	v_cvt_f32_ubyte0_e32 v85, v29
	v_cvt_f32_ubyte1_e32 v86, v29
	v_cvt_f32_ubyte2_e32 v87, v29
	v_cvt_f32_ubyte3_e32 v88, v29
	v_fmac_f32_e32 v6, v85, v54
	v_fmac_f32_e32 v7, v86, v54
	v_fmac_f32_e32 v8, v87, v54
	v_fmac_f32_e32 v9, v88, v54
	v_cvt_f32_ubyte0_e32 v85, v30
	v_cvt_f32_ubyte1_e32 v86, v30
	v_cvt_f32_ubyte2_e32 v87, v30
	v_cvt_f32_ubyte3_e32 v88, v30
	v_fmac_f32_e32 v10, v85, v54
	v_fmac_f32_e32 v11, v86, v54
	v_fmac_f32_e32 v12, v87, v54
	v_fmac_f32_e32 v13, v88, v54
	v_cvt_f32_ubyte0_e32 v85, v31
	v_cvt_f32_ubyte1_e32 v86, v31
	v_cvt_f32_ubyte2_e32 v87, v31
	v_cvt_f32_ubyte3_e32 v88, v31
	v_fmac_f32_e32 v14, v85, v54
	v_fmac_f32_e32 v15, v86, v54
	v_fmac_f32_e32 v16, v87, v54
	v_fmac_f32_e32 v17, v88, v54
	v_add_f32_e32 v18, v18, v54
	v_and_b32_e32 v84, 0xffff, v80
	v_lshl_or_b32 v83, v84, 7, v89
	v_cmp_lt_i32_e32 vcc, 18, v78
	s_mov_b64 exec, vcc
	global_load_dwordx4 v[28:31], v83, s[12:13]
	s_mov_b64 exec, -1
	v_lshlrev_b32_e32 v109, 1, v84
	global_load_ushort v54, v109, s[14:15]
	s_waitcnt vmcnt(6)
	v_cvt_f32_f16_e32 v55, v55
	v_cvt_f32_ubyte0_e32 v85, v32
	v_cvt_f32_ubyte1_e32 v86, v32
	v_cvt_f32_ubyte2_e32 v87, v32
	v_cvt_f32_ubyte3_e32 v88, v32
	v_fmac_f32_e32 v2, v85, v55
	v_fmac_f32_e32 v3, v86, v55
	v_fmac_f32_e32 v4, v87, v55
	v_fmac_f32_e32 v5, v88, v55
	v_cvt_f32_ubyte0_e32 v85, v33
	v_cvt_f32_ubyte1_e32 v86, v33
	v_cvt_f32_ubyte2_e32 v87, v33
	v_cvt_f32_ubyte3_e32 v88, v33
	v_fmac_f32_e32 v6, v85, v55
	v_fmac_f32_e32 v7, v86, v55
	v_fmac_f32_e32 v8, v87, v55
	v_fmac_f32_e32 v9, v88, v55
	v_cvt_f32_ubyte0_e32 v85, v34
	v_cvt_f32_ubyte1_e32 v86, v34
	v_cvt_f32_ubyte2_e32 v87, v34
	v_cvt_f32_ubyte3_e32 v88, v34
	v_fmac_f32_e32 v10, v85, v55
	v_fmac_f32_e32 v11, v86, v55
	v_fmac_f32_e32 v12, v87, v55
	v_fmac_f32_e32 v13, v88, v55
	v_cvt_f32_ubyte0_e32 v85, v35
	v_cvt_f32_ubyte1_e32 v86, v35
	v_cvt_f32_ubyte2_e32 v87, v35
	v_cvt_f32_ubyte3_e32 v88, v35
	v_fmac_f32_e32 v14, v85, v55
	v_fmac_f32_e32 v15, v86, v55
	v_fmac_f32_e32 v16, v87, v55
	v_fmac_f32_e32 v17, v88, v55
	v_add_f32_e32 v18, v18, v55
	v_lshrrev_b32_e32 v84, 16, v80
	v_lshl_or_b32 v83, v84, 7, v89
	v_cmp_lt_i32_e32 vcc, 19, v78
	s_mov_b64 exec, vcc
	global_load_dwordx4 v[32:35], v83, s[12:13]
	s_mov_b64 exec, -1
	v_lshlrev_b32_e32 v109, 1, v84
	global_load_ushort v55, v109, s[14:15]
	s_cmp_le_u32 s40, 20
	s_cbranch_scc1 .Lg1_tail0
	s_waitcnt lgkmcnt(0)
	ds_bpermute_b32 v80, v90, v74 offset:12
	s_waitcnt vmcnt(6)
	v_cvt_f32_f16_e32 v52, v52
	v_cvt_f32_ubyte0_e32 v85, v20
	v_cvt_f32_ubyte1_e32 v86, v20
	v_cvt_f32_ubyte2_e32 v87, v20
	v_cvt_f32_ubyte3_e32 v88, v20
	v_fmac_f32_e32 v2, v85, v52
	v_fmac_f32_e32 v3, v86, v52
	v_fmac_f32_e32 v4, v87, v52
	v_fmac_f32_e32 v5, v88, v52
	v_cvt_f32_ubyte0_e32 v85, v21
	v_cvt_f32_ubyte1_e32 v86, v21
	v_cvt_f32_ubyte2_e32 v87, v21
	v_cvt_f32_ubyte3_e32 v88, v21
	v_fmac_f32_e32 v6, v85, v52
	v_fmac_f32_e32 v7, v86, v52
	v_fmac_f32_e32 v8, v87, v52
	v_fmac_f32_e32 v9, v88, v52
	v_cvt_f32_ubyte0_e32 v85, v22
	v_cvt_f32_ubyte1_e32 v86, v22
	v_cvt_f32_ubyte2_e32 v87, v22
	v_cvt_f32_ubyte3_e32 v88, v22
	v_fmac_f32_e32 v10, v85, v52
	v_fmac_f32_e32 v11, v86, v52
	v_fmac_f32_e32 v12, v87, v52
	v_fmac_f32_e32 v13, v88, v52
	v_cvt_f32_ubyte0_e32 v85, v23
	v_cvt_f32_ubyte1_e32 v86, v23
	v_cvt_f32_ubyte2_e32 v87, v23
	v_cvt_f32_ubyte3_e32 v88, v23
	v_fmac_f32_e32 v14, v85, v52
	v_fmac_f32_e32 v15, v86, v52
	v_fmac_f32_e32 v16, v87, v52
	v_fmac_f32_e32 v17, v88, v52
	v_add_f32_e32 v18, v18, v52
	v_and_b32_e32 v84, 0xffff, v79
	v_lshl_or_b32 v83, v84, 7, v89
	v_cmp_lt_i32_e32 vcc, 20, v78
	s_mov_b64 exec, vcc
	global_load_dwordx4 v[20:23], v83, s[12:13]
	s_mov_b64 exec, -1
	v_lshlrev_b32_e32 v109, 1, v84
	global_load_ushort v52, v109, s[14:15]
	s_waitcnt vmcnt(6)
	v_cvt_f32_f16_e32 v53, v53
	v_cvt_f32_ubyte0_e32 v85, v24
	v_cvt_f32_ubyte1_e32 v86, v24
	v_cvt_f32_ubyte2_e32 v87, v24
	v_cvt_f32_ubyte3_e32 v88, v24
	v_fmac_f32_e32 v2, v85, v53
	v_fmac_f32_e32 v3, v86, v53
	v_fmac_f32_e32 v4, v87, v53
	v_fmac_f32_e32 v5, v88, v53
	v_cvt_f32_ubyte0_e32 v85, v25
	v_cvt_f32_ubyte1_e32 v86, v25
	v_cvt_f32_ubyte2_e32 v87, v25
	v_cvt_f32_ubyte3_e32 v88, v25
	v_fmac_f32_e32 v6, v85, v53
	v_fmac_f32_e32 v7, v86, v53
	v_fmac_f32_e32 v8, v87, v53
	v_fmac_f32_e32 v9, v88, v53
	v_cvt_f32_ubyte0_e32 v85, v26
	v_cvt_f32_ubyte1_e32 v86, v26
	v_cvt_f32_ubyte2_e32 v87, v26
	v_cvt_f32_ubyte3_e32 v88, v26
	v_fmac_f32_e32 v10, v85, v53
	v_fmac_f32_e32 v11, v86, v53
	v_fmac_f32_e32 v12, v87, v53
	v_fmac_f32_e32 v13, v88, v53
	v_cvt_f32_ubyte0_e32 v85, v27
	v_cvt_f32_ubyte1_e32 v86, v27
	v_cvt_f32_ubyte2_e32 v87, v27
	v_cvt_f32_ubyte3_e32 v88, v27
	v_fmac_f32_e32 v14, v85, v53
	v_fmac_f32_e32 v15, v86, v53
	v_fmac_f32_e32 v16, v87, v53
	v_fmac_f32_e32 v17, v88, v53
	v_add_f32_e32 v18, v18, v53
	v_lshrrev_b32_e32 v84, 16, v79
	v_lshl_or_b32 v83, v84, 7, v89
	v_cmp_lt_i32_e32 vcc, 21, v78
	s_mov_b64 exec, vcc
	global_load_dwordx4 v[24:27], v83, s[12:13]
	s_mov_b64 exec, -1
	v_lshlrev_b32_e32 v109, 1, v84
	global_load_ushort v53, v109, s[14:15]
	s_waitcnt lgkmcnt(0)
	ds_bpermute_b32 v79, v90, v74 offset:16
	s_waitcnt vmcnt(6)
	v_cvt_f32_f16_e32 v54, v54
	v_cvt_f32_ubyte0_e32 v85, v28
	v_cvt_f32_ubyte1_e32 v86, v28
	v_cvt_f32_ubyte2_e32 v87, v28
	v_cvt_f32_ubyte3_e32 v88, v28
	v_fmac_f32_e32 v2, v85, v54
	v_fmac_f32_e32 v3, v86, v54
	v_fmac_f32_e32 v4, v87, v54
	v_fmac_f32_e32 v5, v88, v54
	v_cvt_f32_ubyte0_e32 v85, v29
	v_cvt_f32_ubyte1_e32 v86, v29
	v_cvt_f32_ubyte2_e32 v87, v29
	v_cvt_f32_ubyte3_e32 v88, v29
	v_fmac_f32_e32 v6, v85, v54
	v_fmac_f32_e32 v7, v86, v54
	v_fmac_f32_e32 v8, v87, v54
	v_fmac_f32_e32 v9, v88, v54
	v_cvt_f32_ubyte0_e32 v85, v30
	v_cvt_f32_ubyte1_e32 v86, v30
	v_cvt_f32_ubyte2_e32 v87, v30
	v_cvt_f32_ubyte3_e32 v88, v30
	v_fmac_f32_e32 v10, v85, v54
	v_fmac_f32_e32 v11, v86, v54
	v_fmac_f32_e32 v12, v87, v54
	v_fmac_f32_e32 v13, v88, v54
	v_cvt_f32_ubyte0_e32 v85, v31
	v_cvt_f32_ubyte1_e32 v86, v31
	v_cvt_f32_ubyte2_e32 v87, v31
	v_cvt_f32_ubyte3_e32 v88, v31
	v_fmac_f32_e32 v14, v85, v54
	v_fmac_f32_e32 v15, v86, v54
	v_fmac_f32_e32 v16, v87, v54
	v_fmac_f32_e32 v17, v88, v54
	v_add_f32_e32 v18, v18, v54
	v_and_b32_e32 v84, 0xffff, v80
	v_lshl_or_b32 v83, v84, 7, v89
	v_cmp_lt_i32_e32 vcc, 22, v78
	s_mov_b64 exec, vcc
	global_load_dwordx4 v[28:31], v83, s[12:13]
	s_mov_b64 exec, -1
	v_lshlrev_b32_e32 v109, 1, v84
	global_load_ushort v54, v109, s[14:15]
	s_waitcnt vmcnt(6)
	v_cvt_f32_f16_e32 v55, v55
	v_cvt_f32_ubyte0_e32 v85, v32
	v_cvt_f32_ubyte1_e32 v86, v32
	v_cvt_f32_ubyte2_e32 v87, v32
	v_cvt_f32_ubyte3_e32 v88, v32
	v_fmac_f32_e32 v2, v85, v55
	v_fmac_f32_e32 v3, v86, v55
	v_fmac_f32_e32 v4, v87, v55
	v_fmac_f32_e32 v5, v88, v55
	v_cvt_f32_ubyte0_e32 v85, v33
	v_cvt_f32_ubyte1_e32 v86, v33
	v_cvt_f32_ubyte2_e32 v87, v33
	v_cvt_f32_ubyte3_e32 v88, v33
	v_fmac_f32_e32 v6, v85, v55
	v_fmac_f32_e32 v7, v86, v55
	v_fmac_f32_e32 v8, v87, v55
	v_fmac_f32_e32 v9, v88, v55
	v_cvt_f32_ubyte0_e32 v85, v34
	v_cvt_f32_ubyte1_e32 v86, v34
	v_cvt_f32_ubyte2_e32 v87, v34
	v_cvt_f32_ubyte3_e32 v88, v34
	v_fmac_f32_e32 v10, v85, v55
	v_fmac_f32_e32 v11, v86, v55
	v_fmac_f32_e32 v12, v87, v55
	v_fmac_f32_e32 v13, v88, v55
	v_cvt_f32_ubyte0_e32 v85, v35
	v_cvt_f32_ubyte1_e32 v86, v35
	v_cvt_f32_ubyte2_e32 v87, v35
	v_cvt_f32_ubyte3_e32 v88, v35
	v_fmac_f32_e32 v14, v85, v55
	v_fmac_f32_e32 v15, v86, v55
	v_fmac_f32_e32 v16, v87, v55
	v_fmac_f32_e32 v17, v88, v55
	v_add_f32_e32 v18, v18, v55
	v_lshrrev_b32_e32 v84, 16, v80
	v_lshl_or_b32 v83, v84, 7, v89
	v_cmp_lt_i32_e32 vcc, 23, v78
	s_mov_b64 exec, vcc
	global_load_dwordx4 v[32:35], v83, s[12:13]
	s_mov_b64 exec, -1
	v_lshlrev_b32_e32 v109, 1, v84
	global_load_ushort v55, v109, s[14:15]
	s_cmp_le_u32 s40, 24
	s_cbranch_scc1 .Lg1_tail0
	s_waitcnt lgkmcnt(0)
	ds_bpermute_b32 v80, v90, v74 offset:20
	s_waitcnt vmcnt(6)
	v_cvt_f32_f16_e32 v52, v52
	v_cvt_f32_ubyte0_e32 v85, v20
	v_cvt_f32_ubyte1_e32 v86, v20
	v_cvt_f32_ubyte2_e32 v87, v20
	v_cvt_f32_ubyte3_e32 v88, v20
	v_fmac_f32_e32 v2, v85, v52
	v_fmac_f32_e32 v3, v86, v52
	v_fmac_f32_e32 v4, v87, v52
	v_fmac_f32_e32 v5, v88, v52
	v_cvt_f32_ubyte0_e32 v85, v21
	v_cvt_f32_ubyte1_e32 v86, v21
	v_cvt_f32_ubyte2_e32 v87, v21
	v_cvt_f32_ubyte3_e32 v88, v21
	v_fmac_f32_e32 v6, v85, v52
	v_fmac_f32_e32 v7, v86, v52
	v_fmac_f32_e32 v8, v87, v52
	v_fmac_f32_e32 v9, v88, v52
	v_cvt_f32_ubyte0_e32 v85, v22
	v_cvt_f32_ubyte1_e32 v86, v22
	v_cvt_f32_ubyte2_e32 v87, v22
	v_cvt_f32_ubyte3_e32 v88, v22
	v_fmac_f32_e32 v10, v85, v52
	v_fmac_f32_e32 v11, v86, v52
	v_fmac_f32_e32 v12, v87, v52
	v_fmac_f32_e32 v13, v88, v52
	v_cvt_f32_ubyte0_e32 v85, v23
	v_cvt_f32_ubyte1_e32 v86, v23
	v_cvt_f32_ubyte2_e32 v87, v23
	v_cvt_f32_ubyte3_e32 v88, v23
	v_fmac_f32_e32 v14, v85, v52
	v_fmac_f32_e32 v15, v86, v52
	v_fmac_f32_e32 v16, v87, v52
	v_fmac_f32_e32 v17, v88, v52
	v_add_f32_e32 v18, v18, v52
	v_and_b32_e32 v84, 0xffff, v79
	v_lshl_or_b32 v83, v84, 7, v89
	v_cmp_lt_i32_e32 vcc, 24, v78
	s_mov_b64 exec, vcc
	global_load_dwordx4 v[20:23], v83, s[12:13]
	s_mov_b64 exec, -1
	v_lshlrev_b32_e32 v109, 1, v84
	global_load_ushort v52, v109, s[14:15]
	s_waitcnt vmcnt(6)
	v_cvt_f32_f16_e32 v53, v53
	v_cvt_f32_ubyte0_e32 v85, v24
	v_cvt_f32_ubyte1_e32 v86, v24
	v_cvt_f32_ubyte2_e32 v87, v24
	v_cvt_f32_ubyte3_e32 v88, v24
	v_fmac_f32_e32 v2, v85, v53
	v_fmac_f32_e32 v3, v86, v53
	v_fmac_f32_e32 v4, v87, v53
	v_fmac_f32_e32 v5, v88, v53
	v_cvt_f32_ubyte0_e32 v85, v25
	v_cvt_f32_ubyte1_e32 v86, v25
	v_cvt_f32_ubyte2_e32 v87, v25
	v_cvt_f32_ubyte3_e32 v88, v25
	v_fmac_f32_e32 v6, v85, v53
	v_fmac_f32_e32 v7, v86, v53
	v_fmac_f32_e32 v8, v87, v53
	v_fmac_f32_e32 v9, v88, v53
	v_cvt_f32_ubyte0_e32 v85, v26
	v_cvt_f32_ubyte1_e32 v86, v26
	v_cvt_f32_ubyte2_e32 v87, v26
	v_cvt_f32_ubyte3_e32 v88, v26
	v_fmac_f32_e32 v10, v85, v53
	v_fmac_f32_e32 v11, v86, v53
	v_fmac_f32_e32 v12, v87, v53
	v_fmac_f32_e32 v13, v88, v53
	v_cvt_f32_ubyte0_e32 v85, v27
	v_cvt_f32_ubyte1_e32 v86, v27
	v_cvt_f32_ubyte2_e32 v87, v27
	v_cvt_f32_ubyte3_e32 v88, v27
	v_fmac_f32_e32 v14, v85, v53
	v_fmac_f32_e32 v15, v86, v53
	v_fmac_f32_e32 v16, v87, v53
	v_fmac_f32_e32 v17, v88, v53
	v_add_f32_e32 v18, v18, v53
	v_lshrrev_b32_e32 v84, 16, v79
	v_lshl_or_b32 v83, v84, 7, v89
	v_cmp_lt_i32_e32 vcc, 25, v78
	s_mov_b64 exec, vcc
	global_load_dwordx4 v[24:27], v83, s[12:13]
	s_mov_b64 exec, -1
	v_lshlrev_b32_e32 v109, 1, v84
	global_load_ushort v53, v109, s[14:15]
	s_waitcnt lgkmcnt(0)
	ds_bpermute_b32 v79, v90, v74 offset:24
	s_waitcnt vmcnt(6)
	v_cvt_f32_f16_e32 v54, v54
	v_cvt_f32_ubyte0_e32 v85, v28
	v_cvt_f32_ubyte1_e32 v86, v28
	v_cvt_f32_ubyte2_e32 v87, v28
	v_cvt_f32_ubyte3_e32 v88, v28
	v_fmac_f32_e32 v2, v85, v54
	v_fmac_f32_e32 v3, v86, v54
	v_fmac_f32_e32 v4, v87, v54
	v_fmac_f32_e32 v5, v88, v54
	v_cvt_f32_ubyte0_e32 v85, v29
	v_cvt_f32_ubyte1_e32 v86, v29
	v_cvt_f32_ubyte2_e32 v87, v29
	v_cvt_f32_ubyte3_e32 v88, v29
	v_fmac_f32_e32 v6, v85, v54
	v_fmac_f32_e32 v7, v86, v54
	v_fmac_f32_e32 v8, v87, v54
	v_fmac_f32_e32 v9, v88, v54
	v_cvt_f32_ubyte0_e32 v85, v30
	v_cvt_f32_ubyte1_e32 v86, v30
	v_cvt_f32_ubyte2_e32 v87, v30
	v_cvt_f32_ubyte3_e32 v88, v30
	v_fmac_f32_e32 v10, v85, v54
	v_fmac_f32_e32 v11, v86, v54
	v_fmac_f32_e32 v12, v87, v54
	v_fmac_f32_e32 v13, v88, v54
	v_cvt_f32_ubyte0_e32 v85, v31
	v_cvt_f32_ubyte1_e32 v86, v31
	v_cvt_f32_ubyte2_e32 v87, v31
	v_cvt_f32_ubyte3_e32 v88, v31
	v_fmac_f32_e32 v14, v85, v54
	v_fmac_f32_e32 v15, v86, v54
	v_fmac_f32_e32 v16, v87, v54
	v_fmac_f32_e32 v17, v88, v54
	v_add_f32_e32 v18, v18, v54
	v_and_b32_e32 v84, 0xffff, v80
	v_lshl_or_b32 v83, v84, 7, v89
	v_cmp_lt_i32_e32 vcc, 26, v78
	s_mov_b64 exec, vcc
	global_load_dwordx4 v[28:31], v83, s[12:13]
	s_mov_b64 exec, -1
	v_lshlrev_b32_e32 v109, 1, v84
	global_load_ushort v54, v109, s[14:15]
	s_waitcnt vmcnt(6)
	v_cvt_f32_f16_e32 v55, v55
	v_cvt_f32_ubyte0_e32 v85, v32
	v_cvt_f32_ubyte1_e32 v86, v32
	v_cvt_f32_ubyte2_e32 v87, v32
	v_cvt_f32_ubyte3_e32 v88, v32
	v_fmac_f32_e32 v2, v85, v55
	v_fmac_f32_e32 v3, v86, v55
	v_fmac_f32_e32 v4, v87, v55
	v_fmac_f32_e32 v5, v88, v55
	v_cvt_f32_ubyte0_e32 v85, v33
	v_cvt_f32_ubyte1_e32 v86, v33
	v_cvt_f32_ubyte2_e32 v87, v33
	v_cvt_f32_ubyte3_e32 v88, v33
	v_fmac_f32_e32 v6, v85, v55
	v_fmac_f32_e32 v7, v86, v55
	v_fmac_f32_e32 v8, v87, v55
	v_fmac_f32_e32 v9, v88, v55
	v_cvt_f32_ubyte0_e32 v85, v34
	v_cvt_f32_ubyte1_e32 v86, v34
	v_cvt_f32_ubyte2_e32 v87, v34
	v_cvt_f32_ubyte3_e32 v88, v34
	v_fmac_f32_e32 v10, v85, v55
	v_fmac_f32_e32 v11, v86, v55
	v_fmac_f32_e32 v12, v87, v55
	v_fmac_f32_e32 v13, v88, v55
	v_cvt_f32_ubyte0_e32 v85, v35
	v_cvt_f32_ubyte1_e32 v86, v35
	v_cvt_f32_ubyte2_e32 v87, v35
	v_cvt_f32_ubyte3_e32 v88, v35
	v_fmac_f32_e32 v14, v85, v55
	v_fmac_f32_e32 v15, v86, v55
	v_fmac_f32_e32 v16, v87, v55
	v_fmac_f32_e32 v17, v88, v55
	v_add_f32_e32 v18, v18, v55
	v_lshrrev_b32_e32 v84, 16, v80
	v_lshl_or_b32 v83, v84, 7, v89
	v_cmp_lt_i32_e32 vcc, 27, v78
	s_mov_b64 exec, vcc
	global_load_dwordx4 v[32:35], v83, s[12:13]
	s_mov_b64 exec, -1
	v_lshlrev_b32_e32 v109, 1, v84
	global_load_ushort v55, v109, s[14:15]
	s_cmp_le_u32 s40, 28
	s_cbranch_scc1 .Lg1_tail0
	s_waitcnt lgkmcnt(0)
	ds_bpermute_b32 v80, v90, v74 offset:28
	s_waitcnt vmcnt(6)
	v_cvt_f32_f16_e32 v52, v52
	v_cvt_f32_ubyte0_e32 v85, v20
	v_cvt_f32_ubyte1_e32 v86, v20
	v_cvt_f32_ubyte2_e32 v87, v20
	v_cvt_f32_ubyte3_e32 v88, v20
	v_fmac_f32_e32 v2, v85, v52
	v_fmac_f32_e32 v3, v86, v52
	v_fmac_f32_e32 v4, v87, v52
	v_fmac_f32_e32 v5, v88, v52
	v_cvt_f32_ubyte0_e32 v85, v21
	v_cvt_f32_ubyte1_e32 v86, v21
	v_cvt_f32_ubyte2_e32 v87, v21
	v_cvt_f32_ubyte3_e32 v88, v21
	v_fmac_f32_e32 v6, v85, v52
	v_fmac_f32_e32 v7, v86, v52
	v_fmac_f32_e32 v8, v87, v52
	v_fmac_f32_e32 v9, v88, v52
	v_cvt_f32_ubyte0_e32 v85, v22
	v_cvt_f32_ubyte1_e32 v86, v22
	v_cvt_f32_ubyte2_e32 v87, v22
	v_cvt_f32_ubyte3_e32 v88, v22
	v_fmac_f32_e32 v10, v85, v52
	v_fmac_f32_e32 v11, v86, v52
	v_fmac_f32_e32 v12, v87, v52
	v_fmac_f32_e32 v13, v88, v52
	v_cvt_f32_ubyte0_e32 v85, v23
	v_cvt_f32_ubyte1_e32 v86, v23
	v_cvt_f32_ubyte2_e32 v87, v23
	v_cvt_f32_ubyte3_e32 v88, v23
	v_fmac_f32_e32 v14, v85, v52
	v_fmac_f32_e32 v15, v86, v52
	v_fmac_f32_e32 v16, v87, v52
	v_fmac_f32_e32 v17, v88, v52
	v_add_f32_e32 v18, v18, v52
	v_and_b32_e32 v84, 0xffff, v79
	v_lshl_or_b32 v83, v84, 7, v89
	v_cmp_lt_i32_e32 vcc, 28, v78
	s_mov_b64 exec, vcc
	global_load_dwordx4 v[20:23], v83, s[12:13]
	s_mov_b64 exec, -1
	v_lshlrev_b32_e32 v109, 1, v84
	global_load_ushort v52, v109, s[14:15]
	s_waitcnt vmcnt(6)
	v_cvt_f32_f16_e32 v53, v53
	v_cvt_f32_ubyte0_e32 v85, v24
	v_cvt_f32_ubyte1_e32 v86, v24
	v_cvt_f32_ubyte2_e32 v87, v24
	v_cvt_f32_ubyte3_e32 v88, v24
	v_fmac_f32_e32 v2, v85, v53
	v_fmac_f32_e32 v3, v86, v53
	v_fmac_f32_e32 v4, v87, v53
	v_fmac_f32_e32 v5, v88, v53
	v_cvt_f32_ubyte0_e32 v85, v25
	v_cvt_f32_ubyte1_e32 v86, v25
	v_cvt_f32_ubyte2_e32 v87, v25
	v_cvt_f32_ubyte3_e32 v88, v25
	v_fmac_f32_e32 v6, v85, v53
	v_fmac_f32_e32 v7, v86, v53
	v_fmac_f32_e32 v8, v87, v53
	v_fmac_f32_e32 v9, v88, v53
	v_cvt_f32_ubyte0_e32 v85, v26
	v_cvt_f32_ubyte1_e32 v86, v26
	v_cvt_f32_ubyte2_e32 v87, v26
	v_cvt_f32_ubyte3_e32 v88, v26
	v_fmac_f32_e32 v10, v85, v53
	v_fmac_f32_e32 v11, v86, v53
	v_fmac_f32_e32 v12, v87, v53
	v_fmac_f32_e32 v13, v88, v53
	v_cvt_f32_ubyte0_e32 v85, v27
	v_cvt_f32_ubyte1_e32 v86, v27
	v_cvt_f32_ubyte2_e32 v87, v27
	v_cvt_f32_ubyte3_e32 v88, v27
	v_fmac_f32_e32 v14, v85, v53
	v_fmac_f32_e32 v15, v86, v53
	v_fmac_f32_e32 v16, v87, v53
	v_fmac_f32_e32 v17, v88, v53
	v_add_f32_e32 v18, v18, v53
	v_lshrrev_b32_e32 v84, 16, v79
	v_lshl_or_b32 v83, v84, 7, v89
	v_cmp_lt_i32_e32 vcc, 29, v78
	s_mov_b64 exec, vcc
	global_load_dwordx4 v[24:27], v83, s[12:13]
	s_mov_b64 exec, -1
	v_lshlrev_b32_e32 v109, 1, v84
	global_load_ushort v53, v109, s[14:15]
	s_waitcnt lgkmcnt(0)
	s_waitcnt vmcnt(6)
	v_cvt_f32_f16_e32 v54, v54
	v_cvt_f32_ubyte0_e32 v85, v28
	v_cvt_f32_ubyte1_e32 v86, v28
	v_cvt_f32_ubyte2_e32 v87, v28
	v_cvt_f32_ubyte3_e32 v88, v28
	v_fmac_f32_e32 v2, v85, v54
	v_fmac_f32_e32 v3, v86, v54
	v_fmac_f32_e32 v4, v87, v54
	v_fmac_f32_e32 v5, v88, v54
	v_cvt_f32_ubyte0_e32 v85, v29
	v_cvt_f32_ubyte1_e32 v86, v29
	v_cvt_f32_ubyte2_e32 v87, v29
	v_cvt_f32_ubyte3_e32 v88, v29
	v_fmac_f32_e32 v6, v85, v54
	v_fmac_f32_e32 v7, v86, v54
	v_fmac_f32_e32 v8, v87, v54
	v_fmac_f32_e32 v9, v88, v54
	v_cvt_f32_ubyte0_e32 v85, v30
	v_cvt_f32_ubyte1_e32 v86, v30
	v_cvt_f32_ubyte2_e32 v87, v30
	v_cvt_f32_ubyte3_e32 v88, v30
	v_fmac_f32_e32 v10, v85, v54
	v_fmac_f32_e32 v11, v86, v54
	v_fmac_f32_e32 v12, v87, v54
	v_fmac_f32_e32 v13, v88, v54
	v_cvt_f32_ubyte0_e32 v85, v31
	v_cvt_f32_ubyte1_e32 v86, v31
	v_cvt_f32_ubyte2_e32 v87, v31
	v_cvt_f32_ubyte3_e32 v88, v31
	v_fmac_f32_e32 v14, v85, v54
	v_fmac_f32_e32 v15, v86, v54
	v_fmac_f32_e32 v16, v87, v54
	v_fmac_f32_e32 v17, v88, v54
	v_add_f32_e32 v18, v18, v54
	v_and_b32_e32 v84, 0xffff, v80
	v_lshl_or_b32 v83, v84, 7, v89
	v_cmp_lt_i32_e32 vcc, 30, v78
	s_mov_b64 exec, vcc
	global_load_dwordx4 v[28:31], v83, s[12:13]
	s_mov_b64 exec, -1
	v_lshlrev_b32_e32 v109, 1, v84
	global_load_ushort v54, v109, s[14:15]
	s_waitcnt vmcnt(6)
	v_cvt_f32_f16_e32 v55, v55
	v_cvt_f32_ubyte0_e32 v85, v32
	v_cvt_f32_ubyte1_e32 v86, v32
	v_cvt_f32_ubyte2_e32 v87, v32
	v_cvt_f32_ubyte3_e32 v88, v32
	v_fmac_f32_e32 v2, v85, v55
	v_fmac_f32_e32 v3, v86, v55
	v_fmac_f32_e32 v4, v87, v55
	v_fmac_f32_e32 v5, v88, v55
	v_cvt_f32_ubyte0_e32 v85, v33
	v_cvt_f32_ubyte1_e32 v86, v33
	v_cvt_f32_ubyte2_e32 v87, v33
	v_cvt_f32_ubyte3_e32 v88, v33
	v_fmac_f32_e32 v6, v85, v55
	v_fmac_f32_e32 v7, v86, v55
	v_fmac_f32_e32 v8, v87, v55
	v_fmac_f32_e32 v9, v88, v55
	v_cvt_f32_ubyte0_e32 v85, v34
	v_cvt_f32_ubyte1_e32 v86, v34
	v_cvt_f32_ubyte2_e32 v87, v34
	v_cvt_f32_ubyte3_e32 v88, v34
	v_fmac_f32_e32 v10, v85, v55
	v_fmac_f32_e32 v11, v86, v55
	v_fmac_f32_e32 v12, v87, v55
	v_fmac_f32_e32 v13, v88, v55
	v_cvt_f32_ubyte0_e32 v85, v35
	v_cvt_f32_ubyte1_e32 v86, v35
	v_cvt_f32_ubyte2_e32 v87, v35
	v_cvt_f32_ubyte3_e32 v88, v35
	v_fmac_f32_e32 v14, v85, v55
	v_fmac_f32_e32 v15, v86, v55
	v_fmac_f32_e32 v16, v87, v55
	v_fmac_f32_e32 v17, v88, v55
	v_add_f32_e32 v18, v18, v55
	v_lshrrev_b32_e32 v84, 16, v80
	v_lshl_or_b32 v83, v84, 7, v89
	v_cmp_lt_i32_e32 vcc, 31, v78
	s_mov_b64 exec, vcc
	global_load_dwordx4 v[32:35], v83, s[12:13]
	s_mov_b64 exec, -1
	v_lshlrev_b32_e32 v109, 1, v84
	global_load_ushort v55, v109, s[14:15]

.Lg2_active:
	s_mov_b32 s60, 0x00ff00ff
	s_mov_b32 s61, 0x0c030c01
	v_lshrrev_b32_e32 v107, 3, v1
	v_and_b32_e32 v108, 7, v1
	v_and_b32_e32 v105, 15, v1
	v_lshrrev_b32_e32 v106, 4, v1
	s_bfe_u32 s36, s3, 0x10002
	s_lshl_b32 s58, s36, 3
	s_xor_b32 s59, s58, 8
	v_or_b32_e32 v102, s58, v107
	v_or_b32_e32 v103, s59, v107
	v_lshlrev_b32_e32 v89, 4, v108
	v_and_b32_e32 v90, 56, v1
	v_lshlrev_b32_e32 v90, 2, v90
	s_waitcnt lgkmcnt(0)
	s_lshl_b32 s58, s6, 8
	s_add_u32 s32, s16, s58
	s_addc_u32 s33, s17, 0
	s_lshl_b32 s58, s6, 10
	s_add_u32 s34, s18, s58
	s_addc_u32 s35, s19, 0
	v_lshlrev_b32_e32 v109, 4, v105
	global_load_dword v104, v109, s[32:33] offset:8
	v_lshlrev_b32_e32 v110, 4, v102
	global_load_dwordx2 v[68:69], v110, s[32:33]
	v_lshlrev_b32_e32 v111, 4, v103
	global_load_dwordx2 v[70:71], v111, s[32:33]
	v_lshlrev_b32_e32 v101, 2, v108
	v_lshl_or_b32 v110, v102, 6, v101
	global_load_dword v60, v110, s[34:35]
	global_load_dword v61, v110, s[34:35] offset:32
	v_lshl_or_b32 v111, v103, 6, v101
	global_load_dword v62, v111, s[34:35]
	global_load_dword v63, v111, s[34:35] offset:32
	global_load_dwordx4 v[2:5], v95, s[22:23]
	global_load_dwordx4 v[6:9], v98, s[22:23]
	global_load_dwordx4 v[10:13], v99, s[22:23]
	global_load_dwordx4 v[14:17], v100, s[22:23]
	v_and_b32_e32 v101, 0x7f, v0
	v_lshlrev_b32_e32 v101, 2, v101
	global_load_dword v19, v101, s[24:25]
	s_mul_i32 s48, s3, 0x1100
	s_add_u32 s48, s48, 66048
	v_mul_u32_u24_e32 v91, 0x110, v102
	v_lshl_add_u32 v91, v108, 5, v91
	v_add_u32_e32 v91, s48, v91
	v_mul_u32_u24_e32 v92, 0x110, v103
	v_lshl_add_u32 v92, v108, 5, v92
	v_add_u32_e32 v92, s48, v92
	s_waitcnt vmcnt(5)
	v_readlane_b32 s49, v69, 0
	v_readlane_b32 s50, v69, 8
	v_readlane_b32 s51, v69, 16
	v_readlane_b32 s52, v69, 24
	v_readlane_b32 s53, v69, 32
	v_readlane_b32 s54, v69, 40
	v_readlane_b32 s55, v69, 48
	v_readlane_b32 s56, v69, 56
	s_max_i32 s37, s49, s50
	s_max_i32 s37, s37, s51
	s_max_i32 s37, s37, s52
	s_max_i32 s37, s37, s53
	s_max_i32 s37, s37, s54
	s_max_i32 s37, s37, s55
	s_max_i32 s37, s37, s56
	v_readlane_b32 s49, v71, 0
	v_readlane_b32 s50, v71, 8
	v_readlane_b32 s51, v71, 16
	v_readlane_b32 s52, v71, 24
	v_readlane_b32 s53, v71, 32
	v_readlane_b32 s54, v71, 40
	v_readlane_b32 s55, v71, 48
	v_readlane_b32 s56, v71, 56
	s_max_i32 s38, s49, s50
	s_max_i32 s38, s38, s51
	s_max_i32 s38, s38, s52
	s_max_i32 s38, s38, s53
	s_max_i32 s38, s38, s54
	s_max_i32 s38, s38, s55
	s_max_i32 s38, s38, s56
	v_lshlrev_b32_e32 v103, 8, v104
	v_lshl_or_b32 v103, v106, 4, v103
	s_waitcnt vmcnt(0)
	ds_write_b128 v96, v[2:5]
	ds_write_b128 v96, v[6:9] offset:16384
	ds_write_b128 v96, v[10:13] offset:32768
	ds_write_b128 v96, v[14:17] offset:49152
	v_add_u32_e32 v101, 0x10000, v101
	ds_write_b32 v101, v19
	s_mov_b32 s39, 0

.Lg2_sel_done:
	s_min_i32 s40, s41, 32
	s_add_i32 s40, s40, 3
	s_and_b32 s40, s40, 0x3c
	s_max_i32 s40, s40, 4
	v_mov_b32_e32 v2, 0
	v_mov_b32_e32 v3, 0
	v_mov_b32_e32 v4, 0
	v_mov_b32_e32 v5, 0
	v_mov_b32_e32 v6, 0
	v_mov_b32_e32 v7, 0
	v_mov_b32_e32 v8, 0
	v_mov_b32_e32 v9, 0
	v_mov_b32_e32 v10, 0
	v_mov_b32_e32 v11, 0
	v_mov_b32_e32 v12, 0
	v_mov_b32_e32 v13, 0
	v_mov_b32_e32 v14, 0
	v_mov_b32_e32 v15, 0
	v_mov_b32_e32 v16, 0
	v_mov_b32_e32 v17, 0
	s_waitcnt lgkmcnt(0)
	ds_bpermute_b32 v94, v90, v73 offset:0
	ds_bpermute_b32 v95, v90, v73 offset:4
	ds_bpermute_b32 v79, v90, v73 offset:8
	s_waitcnt lgkmcnt(1)
	v_and_b32_e32 v84, 0xffff, v94
	v_lshl_or_b32 v83, v84, 7, v89
	v_cmp_lt_i32_e32 vcc, 0, v78
	s_mov_b64 exec, vcc
	global_load_dwordx4 v[20:23], v83, s[12:13]
	s_mov_b64 exec, -1
	v_lshlrev_b32_e32 v109, 1, v84
	global_load_ushort v52, v109, s[14:15]
	v_lshrrev_b32_e32 v84, 16, v94
	v_lshl_or_b32 v83, v84, 7, v89
	v_cmp_lt_i32_e32 vcc, 1, v78
	s_mov_b64 exec, vcc
	global_load_dwordx4 v[24:27], v83, s[12:13]
	s_mov_b64 exec, -1
	v_lshlrev_b32_e32 v109, 1, v84
	global_load_ushort v53, v109, s[14:15]
	v_and_b32_e32 v84, 0xffff, v95
	v_lshl_or_b32 v83, v84, 7, v89
	v_cmp_lt_i32_e32 vcc, 2, v78
	s_mov_b64 exec, vcc
	global_load_dwordx4 v[28:31], v83, s[12:13]
	s_mov_b64 exec, -1
	v_lshlrev_b32_e32 v109, 1, v84
	global_load_ushort v54, v109, s[14:15]
	v_lshrrev_b32_e32 v84, 16, v95
	v_lshl_or_b32 v83, v84, 7, v89
	v_cmp_lt_i32_e32 vcc, 3, v78
	s_mov_b64 exec, vcc
	global_load_dwordx4 v[32:35], v83, s[12:13]
	s_mov_b64 exec, -1
	v_lshlrev_b32_e32 v109, 1, v84
	global_load_ushort v55, v109, s[14:15]
	s_cmp_eq_u32 s39, 0
	s_cbranch_scc0 .Lg2_nobar
	s_waitcnt lgkmcnt(0)
	s_barrier
.Lg2_nobar:
	s_cmp_le_u32 s40, 4
	s_cbranch_scc1 .Lg2_tail0
	s_waitcnt lgkmcnt(0)
	ds_bpermute_b32 v80, v90, v73 offset:12
	s_waitcnt vmcnt(6)
	v_cvt_f32_f16_e32 v52, v52
	v_cvt_f32_ubyte0_e32 v85, v20
	v_cvt_f32_ubyte1_e32 v86, v20
	v_cvt_f32_ubyte2_e32 v87, v20
	v_cvt_f32_ubyte3_e32 v88, v20
	v_fmac_f32_e32 v2, v85, v52
	v_fmac_f32_e32 v3, v86, v52
	v_fmac_f32_e32 v4, v87, v52
	v_fmac_f32_e32 v5, v88, v52
	v_cvt_f32_ubyte0_e32 v85, v21
	v_cvt_f32_ubyte1_e32 v86, v21
	v_cvt_f32_ubyte2_e32 v87, v21
	v_cvt_f32_ubyte3_e32 v88, v21
	v_fmac_f32_e32 v6, v85, v52
	v_fmac_f32_e32 v7, v86, v52
	v_fmac_f32_e32 v8, v87, v52
	v_fmac_f32_e32 v9, v88, v52
	v_cvt_f32_ubyte0_e32 v85, v22
	v_cvt_f32_ubyte1_e32 v86, v22
	v_cvt_f32_ubyte2_e32 v87, v22
	v_cvt_f32_ubyte3_e32 v88, v22
	v_fmac_f32_e32 v10, v85, v52
	v_fmac_f32_e32 v11, v86, v52
	v_fmac_f32_e32 v12, v87, v52
	v_fmac_f32_e32 v13, v88, v52
	v_cvt_f32_ubyte0_e32 v85, v23
	v_cvt_f32_ubyte1_e32 v86, v23
	v_cvt_f32_ubyte2_e32 v87, v23
	v_cvt_f32_ubyte3_e32 v88, v23
	v_fmac_f32_e32 v14, v85, v52
	v_fmac_f32_e32 v15, v86, v52
	v_fmac_f32_e32 v16, v87, v52
	v_fmac_f32_e32 v17, v88, v52
	v_and_b32_e32 v84, 0xffff, v79
	v_lshl_or_b32 v83, v84, 7, v89
	v_cmp_lt_i32_e32 vcc, 4, v78
	s_mov_b64 exec, vcc
	global_load_dwordx4 v[20:23], v83, s[12:13]
	s_mov_b64 exec, -1
	v_lshlrev_b32_e32 v109, 1, v84
	global_load_ushort v52, v109, s[14:15]
	s_waitcnt vmcnt(6)
	v_cvt_f32_f16_e32 v53, v53
	v_cvt_f32_ubyte0_e32 v85, v24
	v_cvt_f32_ubyte1_e32 v86, v24
	v_cvt_f32_ubyte2_e32 v87, v24
	v_cvt_f32_ubyte3_e32 v88, v24
	v_fmac_f32_e32 v2, v85, v53
	v_fmac_f32_e32 v3, v86, v53
	v_fmac_f32_e32 v4, v87, v53
	v_fmac_f32_e32 v5, v88, v53
	v_cvt_f32_ubyte0_e32 v85, v25
	v_cvt_f32_ubyte1_e32 v86, v25
	v_cvt_f32_ubyte2_e32 v87, v25
	v_cvt_f32_ubyte3_e32 v88, v25
	v_fmac_f32_e32 v6, v85, v53
	v_fmac_f32_e32 v7, v86, v53
	v_fmac_f32_e32 v8, v87, v53
	v_fmac_f32_e32 v9, v88, v53
	v_cvt_f32_ubyte0_e32 v85, v26
	v_cvt_f32_ubyte1_e32 v86, v26
	v_cvt_f32_ubyte2_e32 v87, v26
	v_cvt_f32_ubyte3_e32 v88, v26
	v_fmac_f32_e32 v10, v85, v53
	v_fmac_f32_e32 v11, v86, v53
	v_fmac_f32_e32 v12, v87, v53
	v_fmac_f32_e32 v13, v88, v53
	v_cvt_f32_ubyte0_e32 v85, v27
	v_cvt_f32_ubyte1_e32 v86, v27
	v_cvt_f32_ubyte2_e32 v87, v27
	v_cvt_f32_ubyte3_e32 v88, v27
	v_fmac_f32_e32 v14, v85, v53
	v_fmac_f32_e32 v15, v86, v53
	v_fmac_f32_e32 v16, v87, v53
	v_fmac_f32_e32 v17, v88, v53
	v_lshrrev_b32_e32 v84, 16, v79
	v_lshl_or_b32 v83, v84, 7, v89
	v_cmp_lt_i32_e32 vcc, 5, v78
	s_mov_b64 exec, vcc
	global_load_dwordx4 v[24:27], v83, s[12:13]
	s_mov_b64 exec, -1
	v_lshlrev_b32_e32 v109, 1, v84
	global_load_ushort v53, v109, s[14:15]
	s_waitcnt lgkmcnt(0)
	ds_bpermute_b32 v79, v90, v73 offset:16
	s_waitcnt vmcnt(6)
	v_cvt_f32_f16_e32 v54, v54
	v_cvt_f32_ubyte0_e32 v85, v28
	v_cvt_f32_ubyte1_e32 v86, v28
	v_cvt_f32_ubyte2_e32 v87, v28
	v_cvt_f32_ubyte3_e32 v88, v28
	v_fmac_f32_e32 v2, v85, v54
	v_fmac_f32_e32 v3, v86, v54
	v_fmac_f32_e32 v4, v87, v54
	v_fmac_f32_e32 v5, v88, v54
	v_cvt_f32_ubyte0_e32 v85, v29
	v_cvt_f32_ubyte1_e32 v86, v29
	v_cvt_f32_ubyte2_e32 v87, v29
	v_cvt_f32_ubyte3_e32 v88, v29
	v_fmac_f32_e32 v6, v85, v54
	v_fmac_f32_e32 v7, v86, v54
	v_fmac_f32_e32 v8, v87, v54
	v_fmac_f32_e32 v9, v88, v54
	v_cvt_f32_ubyte0_e32 v85, v30
	v_cvt_f32_ubyte1_e32 v86, v30
	v_cvt_f32_ubyte2_e32 v87, v30
	v_cvt_f32_ubyte3_e32 v88, v30
	v_fmac_f32_e32 v10, v85, v54
	v_fmac_f32_e32 v11, v86, v54
	v_fmac_f32_e32 v12, v87, v54
	v_fmac_f32_e32 v13, v88, v54
	v_cvt_f32_ubyte0_e32 v85, v31
	v_cvt_f32_ubyte1_e32 v86, v31
	v_cvt_f32_ubyte2_e32 v87, v31
	v_cvt_f32_ubyte3_e32 v88, v31
	v_fmac_f32_e32 v14, v85, v54
	v_fmac_f32_e32 v15, v86, v54
	v_fmac_f32_e32 v16, v87, v54
	v_fmac_f32_e32 v17, v88, v54
	v_and_b32_e32 v84, 0xffff, v80
	v_lshl_or_b32 v83, v84, 7, v89
	v_cmp_lt_i32_e32 vcc, 6, v78
	s_mov_b64 exec, vcc
	global_load_dwordx4 v[28:31], v83, s[12:13]
	s_mov_b64 exec, -1
	v_lshlrev_b32_e32 v109, 1, v84
	global_load_ushort v54, v109, s[14:15]
	s_waitcnt vmcnt(6)
	v_cvt_f32_f16_e32 v55, v55
	v_cvt_f32_ubyte0_e32 v85, v32
	v_cvt_f32_ubyte1_e32 v86, v32
	v_cvt_f32_ubyte2_e32 v87, v32
	v_cvt_f32_ubyte3_e32 v88, v32
	v_fmac_f32_e32 v2, v85, v55
	v_fmac_f32_e32 v3, v86, v55
	v_fmac_f32_e32 v4, v87, v55
	v_fmac_f32_e32 v5, v88, v55
	v_cvt_f32_ubyte0_e32 v85, v33
	v_cvt_f32_ubyte1_e32 v86, v33
	v_cvt_f32_ubyte2_e32 v87, v33
	v_cvt_f32_ubyte3_e32 v88, v33
	v_fmac_f32_e32 v6, v85, v55
	v_fmac_f32_e32 v7, v86, v55
	v_fmac_f32_e32 v8, v87, v55
	v_fmac_f32_e32 v9, v88, v55
	v_cvt_f32_ubyte0_e32 v85, v34
	v_cvt_f32_ubyte1_e32 v86, v34
	v_cvt_f32_ubyte2_e32 v87, v34
	v_cvt_f32_ubyte3_e32 v88, v34
	v_fmac_f32_e32 v10, v85, v55
	v_fmac_f32_e32 v11, v86, v55
	v_fmac_f32_e32 v12, v87, v55
	v_fmac_f32_e32 v13, v88, v55
	v_cvt_f32_ubyte0_e32 v85, v35
	v_cvt_f32_ubyte1_e32 v86, v35
	v_cvt_f32_ubyte2_e32 v87, v35
	v_cvt_f32_ubyte3_e32 v88, v35
	v_fmac_f32_e32 v14, v85, v55
	v_fmac_f32_e32 v15, v86, v55
	v_fmac_f32_e32 v16, v87, v55
	v_fmac_f32_e32 v17, v88, v55
	v_lshrrev_b32_e32 v84, 16, v80
	v_lshl_or_b32 v83, v84, 7, v89
	v_cmp_lt_i32_e32 vcc, 7, v78
	s_mov_b64 exec, vcc
	global_load_dwordx4 v[32:35], v83, s[12:13]
	s_mov_b64 exec, -1
	v_lshlrev_b32_e32 v109, 1, v84
	global_load_ushort v55, v109, s[14:15]
	s_cmp_le_u32 s40, 8
	s_cbranch_scc1 .Lg2_tail0
	s_waitcnt lgkmcnt(0)
	ds_bpermute_b32 v80, v90, v73 offset:20
	s_waitcnt vmcnt(6)
	v_cvt_f32_f16_e32 v52, v52
	v_cvt_f32_ubyte0_e32 v85, v20
	v_cvt_f32_ubyte1_e32 v86, v20
	v_cvt_f32_ubyte2_e32 v87, v20
	v_cvt_f32_ubyte3_e32 v88, v20
	v_fmac_f32_e32 v2, v85, v52
	v_fmac_f32_e32 v3, v86, v52
	v_fmac_f32_e32 v4, v87, v52
	v_fmac_f32_e32 v5, v88, v52
	v_cvt_f32_ubyte0_e32 v85, v21
	v_cvt_f32_ubyte1_e32 v86, v21
	v_cvt_f32_ubyte2_e32 v87, v21
	v_cvt_f32_ubyte3_e32 v88, v21
	v_fmac_f32_e32 v6, v85, v52
	v_fmac_f32_e32 v7, v86, v52
	v_fmac_f32_e32 v8, v87, v52
	v_fmac_f32_e32 v9, v88, v52
	v_cvt_f32_ubyte0_e32 v85, v22
	v_cvt_f32_ubyte1_e32 v86, v22
	v_cvt_f32_ubyte2_e32 v87, v22
	v_cvt_f32_ubyte3_e32 v88, v22
	v_fmac_f32_e32 v10, v85, v52
	v_fmac_f32_e32 v11, v86, v52
	v_fmac_f32_e32 v12, v87, v52
	v_fmac_f32_e32 v13, v88, v52
	v_cvt_f32_ubyte0_e32 v85, v23
	v_cvt_f32_ubyte1_e32 v86, v23
	v_cvt_f32_ubyte2_e32 v87, v23
	v_cvt_f32_ubyte3_e32 v88, v23
	v_fmac_f32_e32 v14, v85, v52
	v_fmac_f32_e32 v15, v86, v52
	v_fmac_f32_e32 v16, v87, v52
	v_fmac_f32_e32 v17, v88, v52
	v_and_b32_e32 v84, 0xffff, v79
	v_lshl_or_b32 v83, v84, 7, v89
	v_cmp_lt_i32_e32 vcc, 8, v78
	s_mov_b64 exec, vcc
	global_load_dwordx4 v[20:23], v83, s[12:13]
	s_mov_b64 exec, -1
	v_lshlrev_b32_e32 v109, 1, v84
	global_load_ushort v52, v109, s[14:15]
	s_waitcnt vmcnt(6)
	v_cvt_f32_f16_e32 v53, v53
	v_cvt_f32_ubyte0_e32 v85, v24
	v_cvt_f32_ubyte1_e32 v86, v24
	v_cvt_f32_ubyte2_e32 v87, v24
	v_cvt_f32_ubyte3_e32 v88, v24
	v_fmac_f32_e32 v2, v85, v53
	v_fmac_f32_e32 v3, v86, v53
	v_fmac_f32_e32 v4, v87, v53
	v_fmac_f32_e32 v5, v88, v53
	v_cvt_f32_ubyte0_e32 v85, v25
	v_cvt_f32_ubyte1_e32 v86, v25
	v_cvt_f32_ubyte2_e32 v87, v25
	v_cvt_f32_ubyte3_e32 v88, v25
	v_fmac_f32_e32 v6, v85, v53
	v_fmac_f32_e32 v7, v86, v53
	v_fmac_f32_e32 v8, v87, v53
	v_fmac_f32_e32 v9, v88, v53
	v_cvt_f32_ubyte0_e32 v85, v26
	v_cvt_f32_ubyte1_e32 v86, v26
	v_cvt_f32_ubyte2_e32 v87, v26
	v_cvt_f32_ubyte3_e32 v88, v26
	v_fmac_f32_e32 v10, v85, v53
	v_fmac_f32_e32 v11, v86, v53
	v_fmac_f32_e32 v12, v87, v53
	v_fmac_f32_e32 v13, v88, v53
	v_cvt_f32_ubyte0_e32 v85, v27
	v_cvt_f32_ubyte1_e32 v86, v27
	v_cvt_f32_ubyte2_e32 v87, v27
	v_cvt_f32_ubyte3_e32 v88, v27
	v_fmac_f32_e32 v14, v85, v53
	v_fmac_f32_e32 v15, v86, v53
	v_fmac_f32_e32 v16, v87, v53
	v_fmac_f32_e32 v17, v88, v53
	v_lshrrev_b32_e32 v84, 16, v79
	v_lshl_or_b32 v83, v84, 7, v89
	v_cmp_lt_i32_e32 vcc, 9, v78
	s_mov_b64 exec, vcc
	global_load_dwordx4 v[24:27], v83, s[12:13]
	s_mov_b64 exec, -1
	v_lshlrev_b32_e32 v109, 1, v84
	global_load_ushort v53, v109, s[14:15]
	s_waitcnt lgkmcnt(0)
	ds_bpermute_b32 v79, v90, v73 offset:24
	s_waitcnt vmcnt(6)
	v_cvt_f32_f16_e32 v54, v54
	v_cvt_f32_ubyte0_e32 v85, v28
	v_cvt_f32_ubyte1_e32 v86, v28
	v_cvt_f32_ubyte2_e32 v87, v28
	v_cvt_f32_ubyte3_e32 v88, v28
	v_fmac_f32_e32 v2, v85, v54
	v_fmac_f32_e32 v3, v86, v54
	v_fmac_f32_e32 v4, v87, v54
	v_fmac_f32_e32 v5, v88, v54
	v_cvt_f32_ubyte0_e32 v85, v29
	v_cvt_f32_ubyte1_e32 v86, v29
	v_cvt_f32_ubyte2_e32 v87, v29
	v_cvt_f32_ubyte3_e32 v88, v29
	v_fmac_f32_e32 v6, v85, v54
	v_fmac_f32_e32 v7, v86, v54
	v_fmac_f32_e32 v8, v87, v54
	v_fmac_f32_e32 v9, v88, v54
	v_cvt_f32_ubyte0_e32 v85, v30
	v_cvt_f32_ubyte1_e32 v86, v30
	v_cvt_f32_ubyte2_e32 v87, v30
	v_cvt_f32_ubyte3_e32 v88, v30
	v_fmac_f32_e32 v10, v85, v54
	v_fmac_f32_e32 v11, v86, v54
	v_fmac_f32_e32 v12, v87, v54
	v_fmac_f32_e32 v13, v88, v54
	v_cvt_f32_ubyte0_e32 v85, v31
	v_cvt_f32_ubyte1_e32 v86, v31
	v_cvt_f32_ubyte2_e32 v87, v31
	v_cvt_f32_ubyte3_e32 v88, v31
	v_fmac_f32_e32 v14, v85, v54
	v_fmac_f32_e32 v15, v86, v54
	v_fmac_f32_e32 v16, v87, v54
	v_fmac_f32_e32 v17, v88, v54
	v_and_b32_e32 v84, 0xffff, v80
	v_lshl_or_b32 v83, v84, 7, v89
	v_cmp_lt_i32_e32 vcc, 10, v78
	s_mov_b64 exec, vcc
	global_load_dwordx4 v[28:31], v83, s[12:13]
	s_mov_b64 exec, -1
	v_lshlrev_b32_e32 v109, 1, v84
	global_load_ushort v54, v109, s[14:15]
	s_waitcnt vmcnt(6)
	v_cvt_f32_f16_e32 v55, v55
	v_cvt_f32_ubyte0_e32 v85, v32
	v_cvt_f32_ubyte1_e32 v86, v32
	v_cvt_f32_ubyte2_e32 v87, v32
	v_cvt_f32_ubyte3_e32 v88, v32
	v_fmac_f32_e32 v2, v85, v55
	v_fmac_f32_e32 v3, v86, v55
	v_fmac_f32_e32 v4, v87, v55
	v_fmac_f32_e32 v5, v88, v55
	v_cvt_f32_ubyte0_e32 v85, v33
	v_cvt_f32_ubyte1_e32 v86, v33
	v_cvt_f32_ubyte2_e32 v87, v33
	v_cvt_f32_ubyte3_e32 v88, v33
	v_fmac_f32_e32 v6, v85, v55
	v_fmac_f32_e32 v7, v86, v55
	v_fmac_f32_e32 v8, v87, v55
	v_fmac_f32_e32 v9, v88, v55
	v_cvt_f32_ubyte0_e32 v85, v34
	v_cvt_f32_ubyte1_e32 v86, v34
	v_cvt_f32_ubyte2_e32 v87, v34
	v_cvt_f32_ubyte3_e32 v88, v34
	v_fmac_f32_e32 v10, v85, v55
	v_fmac_f32_e32 v11, v86, v55
	v_fmac_f32_e32 v12, v87, v55
	v_fmac_f32_e32 v13, v88, v55
	v_cvt_f32_ubyte0_e32 v85, v35
	v_cvt_f32_ubyte1_e32 v86, v35
	v_cvt_f32_ubyte2_e32 v87, v35
	v_cvt_f32_ubyte3_e32 v88, v35
	v_fmac_f32_e32 v14, v85, v55
	v_fmac_f32_e32 v15, v86, v55
	v_fmac_f32_e32 v16, v87, v55
	v_fmac_f32_e32 v17, v88, v55
	v_lshrrev_b32_e32 v84, 16, v80
	v_lshl_or_b32 v83, v84, 7, v89
	v_cmp_lt_i32_e32 vcc, 11, v78
	s_mov_b64 exec, vcc
	global_load_dwordx4 v[32:35], v83, s[12:13]
	s_mov_b64 exec, -1
	v_lshlrev_b32_e32 v109, 1, v84
	global_load_ushort v55, v109, s[14:15]
	s_cmp_le_u32 s40, 12
	s_cbranch_scc1 .Lg2_tail0
	s_waitcnt lgkmcnt(0)
	ds_bpermute_b32 v80, v90, v73 offset:28
	s_waitcnt vmcnt(6)
	v_cvt_f32_f16_e32 v52, v52
	v_cvt_f32_ubyte0_e32 v85, v20
	v_cvt_f32_ubyte1_e32 v86, v20
	v_cvt_f32_ubyte2_e32 v87, v20
	v_cvt_f32_ubyte3_e32 v88, v20
	v_fmac_f32_e32 v2, v85, v52
	v_fmac_f32_e32 v3, v86, v52
	v_fmac_f32_e32 v4, v87, v52
	v_fmac_f32_e32 v5, v88, v52
	v_cvt_f32_ubyte0_e32 v85, v21
	v_cvt_f32_ubyte1_e32 v86, v21
	v_cvt_f32_ubyte2_e32 v87, v21
	v_cvt_f32_ubyte3_e32 v88, v21
	v_fmac_f32_e32 v6, v85, v52
	v_fmac_f32_e32 v7, v86, v52
	v_fmac_f32_e32 v8, v87, v52
	v_fmac_f32_e32 v9, v88, v52
	v_cvt_f32_ubyte0_e32 v85, v22
	v_cvt_f32_ubyte1_e32 v86, v22
	v_cvt_f32_ubyte2_e32 v87, v22
	v_cvt_f32_ubyte3_e32 v88, v22
	v_fmac_f32_e32 v10, v85, v52
	v_fmac_f32_e32 v11, v86, v52
	v_fmac_f32_e32 v12, v87, v52
	v_fmac_f32_e32 v13, v88, v52
	v_cvt_f32_ubyte0_e32 v85, v23
	v_cvt_f32_ubyte1_e32 v86, v23
	v_cvt_f32_ubyte2_e32 v87, v23
	v_cvt_f32_ubyte3_e32 v88, v23
	v_fmac_f32_e32 v14, v85, v52
	v_fmac_f32_e32 v15, v86, v52
	v_fmac_f32_e32 v16, v87, v52
	v_fmac_f32_e32 v17, v88, v52
	v_and_b32_e32 v84, 0xffff, v79
	v_lshl_or_b32 v83, v84, 7, v89
	v_cmp_lt_i32_e32 vcc, 12, v78
	s_mov_b64 exec, vcc
	global_load_dwordx4 v[20:23], v83, s[12:13]
	s_mov_b64 exec, -1
	v_lshlrev_b32_e32 v109, 1, v84
	global_load_ushort v52, v109, s[14:15]
	s_waitcnt vmcnt(6)
	v_cvt_f32_f16_e32 v53, v53
	v_cvt_f32_ubyte0_e32 v85, v24
	v_cvt_f32_ubyte1_e32 v86, v24
	v_cvt_f32_ubyte2_e32 v87, v24
	v_cvt_f32_ubyte3_e32 v88, v24
	v_fmac_f32_e32 v2, v85, v53
	v_fmac_f32_e32 v3, v86, v53
	v_fmac_f32_e32 v4, v87, v53
	v_fmac_f32_e32 v5, v88, v53
	v_cvt_f32_ubyte0_e32 v85, v25
	v_cvt_f32_ubyte1_e32 v86, v25
	v_cvt_f32_ubyte2_e32 v87, v25
	v_cvt_f32_ubyte3_e32 v88, v25
	v_fmac_f32_e32 v6, v85, v53
	v_fmac_f32_e32 v7, v86, v53
	v_fmac_f32_e32 v8, v87, v53
	v_fmac_f32_e32 v9, v88, v53
	v_cvt_f32_ubyte0_e32 v85, v26
	v_cvt_f32_ubyte1_e32 v86, v26
	v_cvt_f32_ubyte2_e32 v87, v26
	v_cvt_f32_ubyte3_e32 v88, v26
	v_fmac_f32_e32 v10, v85, v53
	v_fmac_f32_e32 v11, v86, v53
	v_fmac_f32_e32 v12, v87, v53
	v_fmac_f32_e32 v13, v88, v53
	v_cvt_f32_ubyte0_e32 v85, v27
	v_cvt_f32_ubyte1_e32 v86, v27
	v_cvt_f32_ubyte2_e32 v87, v27
	v_cvt_f32_ubyte3_e32 v88, v27
	v_fmac_f32_e32 v14, v85, v53
	v_fmac_f32_e32 v15, v86, v53
	v_fmac_f32_e32 v16, v87, v53
	v_fmac_f32_e32 v17, v88, v53
	v_lshrrev_b32_e32 v84, 16, v79
	v_lshl_or_b32 v83, v84, 7, v89
	v_cmp_lt_i32_e32 vcc, 13, v78
	s_mov_b64 exec, vcc
	global_load_dwordx4 v[24:27], v83, s[12:13]
	s_mov_b64 exec, -1
	v_lshlrev_b32_e32 v109, 1, v84
	global_load_ushort v53, v109, s[14:15]
	s_waitcnt lgkmcnt(0)
	ds_bpermute_b32 v79, v90, v74 offset:0
	s_waitcnt vmcnt(6)
	v_cvt_f32_f16_e32 v54, v54
	v_cvt_f32_ubyte0_e32 v85, v28
	v_cvt_f32_ubyte1_e32 v86, v28
	v_cvt_f32_ubyte2_e32 v87, v28
	v_cvt_f32_ubyte3_e32 v88, v28
	v_fmac_f32_e32 v2, v85, v54
	v_fmac_f32_e32 v3, v86, v54
	v_fmac_f32_e32 v4, v87, v54
	v_fmac_f32_e32 v5, v88, v54
	v_cvt_f32_ubyte0_e32 v85, v29
	v_cvt_f32_ubyte1_e32 v86, v29
	v_cvt_f32_ubyte2_e32 v87, v29
	v_cvt_f32_ubyte3_e32 v88, v29
	v_fmac_f32_e32 v6, v85, v54
	v_fmac_f32_e32 v7, v86, v54
	v_fmac_f32_e32 v8, v87, v54
	v_fmac_f32_e32 v9, v88, v54
	v_cvt_f32_ubyte0_e32 v85, v30
	v_cvt_f32_ubyte1_e32 v86, v30
	v_cvt_f32_ubyte2_e32 v87, v30
	v_cvt_f32_ubyte3_e32 v88, v30
	v_fmac_f32_e32 v10, v85, v54
	v_fmac_f32_e32 v11, v86, v54
	v_fmac_f32_e32 v12, v87, v54
	v_fmac_f32_e32 v13, v88, v54
	v_cvt_f32_ubyte0_e32 v85, v31
	v_cvt_f32_ubyte1_e32 v86, v31
	v_cvt_f32_ubyte2_e32 v87, v31
	v_cvt_f32_ubyte3_e32 v88, v31
	v_fmac_f32_e32 v14, v85, v54
	v_fmac_f32_e32 v15, v86, v54
	v_fmac_f32_e32 v16, v87, v54
	v_fmac_f32_e32 v17, v88, v54
	v_and_b32_e32 v84, 0xffff, v80
	v_lshl_or_b32 v83, v84, 7, v89
	v_cmp_lt_i32_e32 vcc, 14, v78
	s_mov_b64 exec, vcc
	global_load_dwordx4 v[28:31], v83, s[12:13]
	s_mov_b64 exec, -1
	v_lshlrev_b32_e32 v109, 1, v84
	global_load_ushort v54, v109, s[14:15]
	s_waitcnt vmcnt(6)
	v_cvt_f32_f16_e32 v55, v55
	v_cvt_f32_ubyte0_e32 v85, v32
	v_cvt_f32_ubyte1_e32 v86, v32
	v_cvt_f32_ubyte2_e32 v87, v32
	v_cvt_f32_ubyte3_e32 v88, v32
	v_fmac_f32_e32 v2, v85, v55
	v_fmac_f32_e32 v3, v86, v55
	v_fmac_f32_e32 v4, v87, v55
	v_fmac_f32_e32 v5, v88, v55
	v_cvt_f32_ubyte0_e32 v85, v33
	v_cvt_f32_ubyte1_e32 v86, v33
	v_cvt_f32_ubyte2_e32 v87, v33
	v_cvt_f32_ubyte3_e32 v88, v33
	v_fmac_f32_e32 v6, v85, v55
	v_fmac_f32_e32 v7, v86, v55
	v_fmac_f32_e32 v8, v87, v55
	v_fmac_f32_e32 v9, v88, v55
	v_cvt_f32_ubyte0_e32 v85, v34
	v_cvt_f32_ubyte1_e32 v86, v34
	v_cvt_f32_ubyte2_e32 v87, v34
	v_cvt_f32_ubyte3_e32 v88, v34
	v_fmac_f32_e32 v10, v85, v55
	v_fmac_f32_e32 v11, v86, v55
	v_fmac_f32_e32 v12, v87, v55
	v_fmac_f32_e32 v13, v88, v55
	v_cvt_f32_ubyte0_e32 v85, v35
	v_cvt_f32_ubyte1_e32 v86, v35
	v_cvt_f32_ubyte2_e32 v87, v35
	v_cvt_f32_ubyte3_e32 v88, v35
	v_fmac_f32_e32 v14, v85, v55
	v_fmac_f32_e32 v15, v86, v55
	v_fmac_f32_e32 v16, v87, v55
	v_fmac_f32_e32 v17, v88, v55
	v_lshrrev_b32_e32 v84, 16, v80
	v_lshl_or_b32 v83, v84, 7, v89
	v_cmp_lt_i32_e32 vcc, 15, v78
	s_mov_b64 exec, vcc
	global_load_dwordx4 v[32:35], v83, s[12:13]
	s_mov_b64 exec, -1
	v_lshlrev_b32_e32 v109, 1, v84
	global_load_ushort v55, v109, s[14:15]
	s_cmp_le_u32 s40, 16
	s_cbranch_scc1 .Lg2_tail0
	s_waitcnt lgkmcnt(0)
	ds_bpermute_b32 v80, v90, v74 offset:4
	s_waitcnt vmcnt(6)
	v_cvt_f32_f16_e32 v52, v52
	v_cvt_f32_ubyte0_e32 v85, v20
	v_cvt_f32_ubyte1_e32 v86, v20
	v_cvt_f32_ubyte2_e32 v87, v20
	v_cvt_f32_ubyte3_e32 v88, v20
	v_fmac_f32_e32 v2, v85, v52
	v_fmac_f32_e32 v3, v86, v52
	v_fmac_f32_e32 v4, v87, v52
	v_fmac_f32_e32 v5, v88, v52
	v_cvt_f32_ubyte0_e32 v85, v21
	v_cvt_f32_ubyte1_e32 v86, v21
	v_cvt_f32_ubyte2_e32 v87, v21
	v_cvt_f32_ubyte3_e32 v88, v21
	v_fmac_f32_e32 v6, v85, v52
	v_fmac_f32_e32 v7, v86, v52
	v_fmac_f32_e32 v8, v87, v52
	v_fmac_f32_e32 v9, v88, v52
	v_cvt_f32_ubyte0_e32 v85, v22
	v_cvt_f32_ubyte1_e32 v86, v22
	v_cvt_f32_ubyte2_e32 v87, v22
	v_cvt_f32_ubyte3_e32 v88, v22
	v_fmac_f32_e32 v10, v85, v52
	v_fmac_f32_e32 v11, v86, v52
	v_fmac_f32_e32 v12, v87, v52
	v_fmac_f32_e32 v13, v88, v52
	v_cvt_f32_ubyte0_e32 v85, v23
	v_cvt_f32_ubyte1_e32 v86, v23
	v_cvt_f32_ubyte2_e32 v87, v23
	v_cvt_f32_ubyte3_e32 v88, v23
	v_fmac_f32_e32 v14, v85, v52
	v_fmac_f32_e32 v15, v86, v52
	v_fmac_f32_e32 v16, v87, v52
	v_fmac_f32_e32 v17, v88, v52
	v_and_b32_e32 v84, 0xffff, v79
	v_lshl_or_b32 v83, v84, 7, v89
	v_cmp_lt_i32_e32 vcc, 16, v78
	s_mov_b64 exec, vcc
	global_load_dwordx4 v[20:23], v83, s[12:13]
	s_mov_b64 exec, -1
	v_lshlrev_b32_e32 v109, 1, v84
	global_load_ushort v52, v109, s[14:15]
	s_waitcnt vmcnt(6)
	v_cvt_f32_f16_e32 v53, v53
	v_cvt_f32_ubyte0_e32 v85, v24
	v_cvt_f32_ubyte1_e32 v86, v24
	v_cvt_f32_ubyte2_e32 v87, v24
	v_cvt_f32_ubyte3_e32 v88, v24
	v_fmac_f32_e32 v2, v85, v53
	v_fmac_f32_e32 v3, v86, v53
	v_fmac_f32_e32 v4, v87, v53
	v_fmac_f32_e32 v5, v88, v53
	v_cvt_f32_ubyte0_e32 v85, v25
	v_cvt_f32_ubyte1_e32 v86, v25
	v_cvt_f32_ubyte2_e32 v87, v25
	v_cvt_f32_ubyte3_e32 v88, v25
	v_fmac_f32_e32 v6, v85, v53
	v_fmac_f32_e32 v7, v86, v53
	v_fmac_f32_e32 v8, v87, v53
	v_fmac_f32_e32 v9, v88, v53
	v_cvt_f32_ubyte0_e32 v85, v26
	v_cvt_f32_ubyte1_e32 v86, v26
	v_cvt_f32_ubyte2_e32 v87, v26
	v_cvt_f32_ubyte3_e32 v88, v26
	v_fmac_f32_e32 v10, v85, v53
	v_fmac_f32_e32 v11, v86, v53
	v_fmac_f32_e32 v12, v87, v53
	v_fmac_f32_e32 v13, v88, v53
	v_cvt_f32_ubyte0_e32 v85, v27
	v_cvt_f32_ubyte1_e32 v86, v27
	v_cvt_f32_ubyte2_e32 v87, v27
	v_cvt_f32_ubyte3_e32 v88, v27
	v_fmac_f32_e32 v14, v85, v53
	v_fmac_f32_e32 v15, v86, v53
	v_fmac_f32_e32 v16, v87, v53
	v_fmac_f32_e32 v17, v88, v53
	v_lshrrev_b32_e32 v84, 16, v79
	v_lshl_or_b32 v83, v84, 7, v89
	v_cmp_lt_i32_e32 vcc, 17, v78
	s_mov_b64 exec, vcc
	global_load_dwordx4 v[24:27], v83, s[12:13]
	s_mov_b64 exec, -1
	v_lshlrev_b32_e32 v109, 1, v84
	global_load_ushort v53, v109, s[14:15]
	s_waitcnt lgkmcnt(0)
	ds_bpermute_b32 v79, v90, v74 offset:8
	s_waitcnt vmcnt(6)
	v_cvt_f32_f16_e32 v54, v54
	v_cvt_f32_ubyte0_e32 v85, v28
	v_cvt_f32_ubyte1_e32 v86, v28
	v_cvt_f32_ubyte2_e32 v87, v28
	v_cvt_f32_ubyte3_e32 v88, v28
	v_fmac_f32_e32 v2, v85, v54
	v_fmac_f32_e32 v3, v86, v54
	v_fmac_f32_e32 v4, v87, v54
	v_fmac_f32_e32 v5, v88, v54
	v_cvt_f32_ubyte0_e32 v85, v29
	v_cvt_f32_ubyte1_e32 v86, v29
	v_cvt_f32_ubyte2_e32 v87, v29
	v_cvt_f32_ubyte3_e32 v88, v29
	v_fmac_f32_e32 v6, v85, v54
	v_fmac_f32_e32 v7, v86, v54
	v_fmac_f32_e32 v8, v87, v54
	v_fmac_f32_e32 v9, v88, v54
	v_cvt_f32_ubyte0_e32 v85, v30
	v_cvt_f32_ubyte1_e32 v86, v30
	v_cvt_f32_ubyte2_e32 v87, v30
	v_cvt_f32_ubyte3_e32 v88, v30
	v_fmac_f32_e32 v10, v85, v54
	v_fmac_f32_e32 v11, v86, v54
	v_fmac_f32_e32 v12, v87, v54
	v_fmac_f32_e32 v13, v88, v54
	v_cvt_f32_ubyte0_e32 v85, v31
	v_cvt_f32_ubyte1_e32 v86, v31
	v_cvt_f32_ubyte2_e32 v87, v31
	v_cvt_f32_ubyte3_e32 v88, v31
	v_fmac_f32_e32 v14, v85, v54
	v_fmac_f32_e32 v15, v86, v54
	v_fmac_f32_e32 v16, v87, v54
	v_fmac_f32_e32 v17, v88, v54
	v_and_b32_e32 v84, 0xffff, v80
	v_lshl_or_b32 v83, v84, 7, v89
	v_cmp_lt_i32_e32 vcc, 18, v78
	s_mov_b64 exec, vcc
	global_load_dwordx4 v[28:31], v83, s[12:13]
	s_mov_b64 exec, -1
	v_lshlrev_b32_e32 v109, 1, v84
	global_load_ushort v54, v109, s[14:15]
	s_waitcnt vmcnt(6)
	v_cvt_f32_f16_e32 v55, v55
	v_cvt_f32_ubyte0_e32 v85, v32
	v_cvt_f32_ubyte1_e32 v86, v32
	v_cvt_f32_ubyte2_e32 v87, v32
	v_cvt_f32_ubyte3_e32 v88, v32
	v_fmac_f32_e32 v2, v85, v55
	v_fmac_f32_e32 v3, v86, v55
	v_fmac_f32_e32 v4, v87, v55
	v_fmac_f32_e32 v5, v88, v55
	v_cvt_f32_ubyte0_e32 v85, v33
	v_cvt_f32_ubyte1_e32 v86, v33
	v_cvt_f32_ubyte2_e32 v87, v33
	v_cvt_f32_ubyte3_e32 v88, v33
	v_fmac_f32_e32 v6, v85, v55
	v_fmac_f32_e32 v7, v86, v55
	v_fmac_f32_e32 v8, v87, v55
	v_fmac_f32_e32 v9, v88, v55
	v_cvt_f32_ubyte0_e32 v85, v34
	v_cvt_f32_ubyte1_e32 v86, v34
	v_cvt_f32_ubyte2_e32 v87, v34
	v_cvt_f32_ubyte3_e32 v88, v34
	v_fmac_f32_e32 v10, v85, v55
	v_fmac_f32_e32 v11, v86, v55
	v_fmac_f32_e32 v12, v87, v55
	v_fmac_f32_e32 v13, v88, v55
	v_cvt_f32_ubyte0_e32 v85, v35
	v_cvt_f32_ubyte1_e32 v86, v35
	v_cvt_f32_ubyte2_e32 v87, v35
	v_cvt_f32_ubyte3_e32 v88, v35
	v_fmac_f32_e32 v14, v85, v55
	v_fmac_f32_e32 v15, v86, v55
	v_fmac_f32_e32 v16, v87, v55
	v_fmac_f32_e32 v17, v88, v55
	v_lshrrev_b32_e32 v84, 16, v80
	v_lshl_or_b32 v83, v84, 7, v89
	v_cmp_lt_i32_e32 vcc, 19, v78
	s_mov_b64 exec, vcc
	global_load_dwordx4 v[32:35], v83, s[12:13]
	s_mov_b64 exec, -1
	v_lshlrev_b32_e32 v109, 1, v84
	global_load_ushort v55, v109, s[14:15]
	s_cmp_le_u32 s40, 20
	s_cbranch_scc1 .Lg2_tail0
	s_waitcnt lgkmcnt(0)
	ds_bpermute_b32 v80, v90, v74 offset:12
	s_waitcnt vmcnt(6)
	v_cvt_f32_f16_e32 v52, v52
	v_cvt_f32_ubyte0_e32 v85, v20
	v_cvt_f32_ubyte1_e32 v86, v20
	v_cvt_f32_ubyte2_e32 v87, v20
	v_cvt_f32_ubyte3_e32 v88, v20
	v_fmac_f32_e32 v2, v85, v52
	v_fmac_f32_e32 v3, v86, v52
	v_fmac_f32_e32 v4, v87, v52
	v_fmac_f32_e32 v5, v88, v52
	v_cvt_f32_ubyte0_e32 v85, v21
	v_cvt_f32_ubyte1_e32 v86, v21
	v_cvt_f32_ubyte2_e32 v87, v21
	v_cvt_f32_ubyte3_e32 v88, v21
	v_fmac_f32_e32 v6, v85, v52
	v_fmac_f32_e32 v7, v86, v52
	v_fmac_f32_e32 v8, v87, v52
	v_fmac_f32_e32 v9, v88, v52
	v_cvt_f32_ubyte0_e32 v85, v22
	v_cvt_f32_ubyte1_e32 v86, v22
	v_cvt_f32_ubyte2_e32 v87, v22
	v_cvt_f32_ubyte3_e32 v88, v22
	v_fmac_f32_e32 v10, v85, v52
	v_fmac_f32_e32 v11, v86, v52
	v_fmac_f32_e32 v12, v87, v52
	v_fmac_f32_e32 v13, v88, v52
	v_cvt_f32_ubyte0_e32 v85, v23
	v_cvt_f32_ubyte1_e32 v86, v23
	v_cvt_f32_ubyte2_e32 v87, v23
	v_cvt_f32_ubyte3_e32 v88, v23
	v_fmac_f32_e32 v14, v85, v52
	v_fmac_f32_e32 v15, v86, v52
	v_fmac_f32_e32 v16, v87, v52
	v_fmac_f32_e32 v17, v88, v52
	v_and_b32_e32 v84, 0xffff, v79
	v_lshl_or_b32 v83, v84, 7, v89
	v_cmp_lt_i32_e32 vcc, 20, v78
	s_mov_b64 exec, vcc
	global_load_dwordx4 v[20:23], v83, s[12:13]
	s_mov_b64 exec, -1
	v_lshlrev_b32_e32 v109, 1, v84
	global_load_ushort v52, v109, s[14:15]
	s_waitcnt vmcnt(6)
	v_cvt_f32_f16_e32 v53, v53
	v_cvt_f32_ubyte0_e32 v85, v24
	v_cvt_f32_ubyte1_e32 v86, v24
	v_cvt_f32_ubyte2_e32 v87, v24
	v_cvt_f32_ubyte3_e32 v88, v24
	v_fmac_f32_e32 v2, v85, v53
	v_fmac_f32_e32 v3, v86, v53
	v_fmac_f32_e32 v4, v87, v53
	v_fmac_f32_e32 v5, v88, v53
	v_cvt_f32_ubyte0_e32 v85, v25
	v_cvt_f32_ubyte1_e32 v86, v25
	v_cvt_f32_ubyte2_e32 v87, v25
	v_cvt_f32_ubyte3_e32 v88, v25
	v_fmac_f32_e32 v6, v85, v53
	v_fmac_f32_e32 v7, v86, v53
	v_fmac_f32_e32 v8, v87, v53
	v_fmac_f32_e32 v9, v88, v53
	v_cvt_f32_ubyte0_e32 v85, v26
	v_cvt_f32_ubyte1_e32 v86, v26
	v_cvt_f32_ubyte2_e32 v87, v26
	v_cvt_f32_ubyte3_e32 v88, v26
	v_fmac_f32_e32 v10, v85, v53
	v_fmac_f32_e32 v11, v86, v53
	v_fmac_f32_e32 v12, v87, v53
	v_fmac_f32_e32 v13, v88, v53
	v_cvt_f32_ubyte0_e32 v85, v27
	v_cvt_f32_ubyte1_e32 v86, v27
	v_cvt_f32_ubyte2_e32 v87, v27
	v_cvt_f32_ubyte3_e32 v88, v27
	v_fmac_f32_e32 v14, v85, v53
	v_fmac_f32_e32 v15, v86, v53
	v_fmac_f32_e32 v16, v87, v53
	v_fmac_f32_e32 v17, v88, v53
	v_lshrrev_b32_e32 v84, 16, v79
	v_lshl_or_b32 v83, v84, 7, v89
	v_cmp_lt_i32_e32 vcc, 21, v78
	s_mov_b64 exec, vcc
	global_load_dwordx4 v[24:27], v83, s[12:13]
	s_mov_b64 exec, -1
	v_lshlrev_b32_e32 v109, 1, v84
	global_load_ushort v53, v109, s[14:15]
	s_waitcnt lgkmcnt(0)
	ds_bpermute_b32 v79, v90, v74 offset:16
	s_waitcnt vmcnt(6)
	v_cvt_f32_f16_e32 v54, v54
	v_cvt_f32_ubyte0_e32 v85, v28
	v_cvt_f32_ubyte1_e32 v86, v28
	v_cvt_f32_ubyte2_e32 v87, v28
	v_cvt_f32_ubyte3_e32 v88, v28
	v_fmac_f32_e32 v2, v85, v54
	v_fmac_f32_e32 v3, v86, v54
	v_fmac_f32_e32 v4, v87, v54
	v_fmac_f32_e32 v5, v88, v54
	v_cvt_f32_ubyte0_e32 v85, v29
	v_cvt_f32_ubyte1_e32 v86, v29
	v_cvt_f32_ubyte2_e32 v87, v29
	v_cvt_f32_ubyte3_e32 v88, v29
	v_fmac_f32_e32 v6, v85, v54
	v_fmac_f32_e32 v7, v86, v54
	v_fmac_f32_e32 v8, v87, v54
	v_fmac_f32_e32 v9, v88, v54
	v_cvt_f32_ubyte0_e32 v85, v30
	v_cvt_f32_ubyte1_e32 v86, v30
	v_cvt_f32_ubyte2_e32 v87, v30
	v_cvt_f32_ubyte3_e32 v88, v30
	v_fmac_f32_e32 v10, v85, v54
	v_fmac_f32_e32 v11, v86, v54
	v_fmac_f32_e32 v12, v87, v54
	v_fmac_f32_e32 v13, v88, v54
	v_cvt_f32_ubyte0_e32 v85, v31
	v_cvt_f32_ubyte1_e32 v86, v31
	v_cvt_f32_ubyte2_e32 v87, v31
	v_cvt_f32_ubyte3_e32 v88, v31
	v_fmac_f32_e32 v14, v85, v54
	v_fmac_f32_e32 v15, v86, v54
	v_fmac_f32_e32 v16, v87, v54
	v_fmac_f32_e32 v17, v88, v54
	v_and_b32_e32 v84, 0xffff, v80
	v_lshl_or_b32 v83, v84, 7, v89
	v_cmp_lt_i32_e32 vcc, 22, v78
	s_mov_b64 exec, vcc
	global_load_dwordx4 v[28:31], v83, s[12:13]
	s_mov_b64 exec, -1
	v_lshlrev_b32_e32 v109, 1, v84
	global_load_ushort v54, v109, s[14:15]
	s_waitcnt vmcnt(6)
	v_cvt_f32_f16_e32 v55, v55
	v_cvt_f32_ubyte0_e32 v85, v32
	v_cvt_f32_ubyte1_e32 v86, v32
	v_cvt_f32_ubyte2_e32 v87, v32
	v_cvt_f32_ubyte3_e32 v88, v32
	v_fmac_f32_e32 v2, v85, v55
	v_fmac_f32_e32 v3, v86, v55
	v_fmac_f32_e32 v4, v87, v55
	v_fmac_f32_e32 v5, v88, v55
	v_cvt_f32_ubyte0_e32 v85, v33
	v_cvt_f32_ubyte1_e32 v86, v33
	v_cvt_f32_ubyte2_e32 v87, v33
	v_cvt_f32_ubyte3_e32 v88, v33
	v_fmac_f32_e32 v6, v85, v55
	v_fmac_f32_e32 v7, v86, v55
	v_fmac_f32_e32 v8, v87, v55
	v_fmac_f32_e32 v9, v88, v55
	v_cvt_f32_ubyte0_e32 v85, v34
	v_cvt_f32_ubyte1_e32 v86, v34
	v_cvt_f32_ubyte2_e32 v87, v34
	v_cvt_f32_ubyte3_e32 v88, v34
	v_fmac_f32_e32 v10, v85, v55
	v_fmac_f32_e32 v11, v86, v55
	v_fmac_f32_e32 v12, v87, v55
	v_fmac_f32_e32 v13, v88, v55
	v_cvt_f32_ubyte0_e32 v85, v35
	v_cvt_f32_ubyte1_e32 v86, v35
	v_cvt_f32_ubyte2_e32 v87, v35
	v_cvt_f32_ubyte3_e32 v88, v35
	v_fmac_f32_e32 v14, v85, v55
	v_fmac_f32_e32 v15, v86, v55
	v_fmac_f32_e32 v16, v87, v55
	v_fmac_f32_e32 v17, v88, v55
	v_lshrrev_b32_e32 v84, 16, v80
	v_lshl_or_b32 v83, v84, 7, v89
	v_cmp_lt_i32_e32 vcc, 23, v78
	s_mov_b64 exec, vcc
	global_load_dwordx4 v[32:35], v83, s[12:13]
	s_mov_b64 exec, -1
	v_lshlrev_b32_e32 v109, 1, v84
	global_load_ushort v55, v109, s[14:15]
	s_cmp_le_u32 s40, 24
	s_cbranch_scc1 .Lg2_tail0
	s_waitcnt lgkmcnt(0)
	ds_bpermute_b32 v80, v90, v74 offset:20
	s_waitcnt vmcnt(6)
	v_cvt_f32_f16_e32 v52, v52
	v_cvt_f32_ubyte0_e32 v85, v20
	v_cvt_f32_ubyte1_e32 v86, v20
	v_cvt_f32_ubyte2_e32 v87, v20
	v_cvt_f32_ubyte3_e32 v88, v20
	v_fmac_f32_e32 v2, v85, v52
	v_fmac_f32_e32 v3, v86, v52
	v_fmac_f32_e32 v4, v87, v52
	v_fmac_f32_e32 v5, v88, v52
	v_cvt_f32_ubyte0_e32 v85, v21
	v_cvt_f32_ubyte1_e32 v86, v21
	v_cvt_f32_ubyte2_e32 v87, v21
	v_cvt_f32_ubyte3_e32 v88, v21
	v_fmac_f32_e32 v6, v85, v52
	v_fmac_f32_e32 v7, v86, v52
	v_fmac_f32_e32 v8, v87, v52
	v_fmac_f32_e32 v9, v88, v52
	v_cvt_f32_ubyte0_e32 v85, v22
	v_cvt_f32_ubyte1_e32 v86, v22
	v_cvt_f32_ubyte2_e32 v87, v22
	v_cvt_f32_ubyte3_e32 v88, v22
	v_fmac_f32_e32 v10, v85, v52
	v_fmac_f32_e32 v11, v86, v52
	v_fmac_f32_e32 v12, v87, v52
	v_fmac_f32_e32 v13, v88, v52
	v_cvt_f32_ubyte0_e32 v85, v23
	v_cvt_f32_ubyte1_e32 v86, v23
	v_cvt_f32_ubyte2_e32 v87, v23
	v_cvt_f32_ubyte3_e32 v88, v23
	v_fmac_f32_e32 v14, v85, v52
	v_fmac_f32_e32 v15, v86, v52
	v_fmac_f32_e32 v16, v87, v52
	v_fmac_f32_e32 v17, v88, v52
	v_and_b32_e32 v84, 0xffff, v79
	v_lshl_or_b32 v83, v84, 7, v89
	v_cmp_lt_i32_e32 vcc, 24, v78
	s_mov_b64 exec, vcc
	global_load_dwordx4 v[20:23], v83, s[12:13]
	s_mov_b64 exec, -1
	v_lshlrev_b32_e32 v109, 1, v84
	global_load_ushort v52, v109, s[14:15]
	s_waitcnt vmcnt(6)
	v_cvt_f32_f16_e32 v53, v53
	v_cvt_f32_ubyte0_e32 v85, v24
	v_cvt_f32_ubyte1_e32 v86, v24
	v_cvt_f32_ubyte2_e32 v87, v24
	v_cvt_f32_ubyte3_e32 v88, v24
	v_fmac_f32_e32 v2, v85, v53
	v_fmac_f32_e32 v3, v86, v53
	v_fmac_f32_e32 v4, v87, v53
	v_fmac_f32_e32 v5, v88, v53
	v_cvt_f32_ubyte0_e32 v85, v25
	v_cvt_f32_ubyte1_e32 v86, v25
	v_cvt_f32_ubyte2_e32 v87, v25
	v_cvt_f32_ubyte3_e32 v88, v25
	v_fmac_f32_e32 v6, v85, v53
	v_fmac_f32_e32 v7, v86, v53
	v_fmac_f32_e32 v8, v87, v53
	v_fmac_f32_e32 v9, v88, v53
	v_cvt_f32_ubyte0_e32 v85, v26
	v_cvt_f32_ubyte1_e32 v86, v26
	v_cvt_f32_ubyte2_e32 v87, v26
	v_cvt_f32_ubyte3_e32 v88, v26
	v_fmac_f32_e32 v10, v85, v53
	v_fmac_f32_e32 v11, v86, v53
	v_fmac_f32_e32 v12, v87, v53
	v_fmac_f32_e32 v13, v88, v53
	v_cvt_f32_ubyte0_e32 v85, v27
	v_cvt_f32_ubyte1_e32 v86, v27
	v_cvt_f32_ubyte2_e32 v87, v27
	v_cvt_f32_ubyte3_e32 v88, v27
	v_fmac_f32_e32 v14, v85, v53
	v_fmac_f32_e32 v15, v86, v53
	v_fmac_f32_e32 v16, v87, v53
	v_fmac_f32_e32 v17, v88, v53
	v_lshrrev_b32_e32 v84, 16, v79
	v_lshl_or_b32 v83, v84, 7, v89
	v_cmp_lt_i32_e32 vcc, 25, v78
	s_mov_b64 exec, vcc
	global_load_dwordx4 v[24:27], v83, s[12:13]
	s_mov_b64 exec, -1
	v_lshlrev_b32_e32 v109, 1, v84
	global_load_ushort v53, v109, s[14:15]
	s_waitcnt lgkmcnt(0)
	ds_bpermute_b32 v79, v90, v74 offset:24
	s_waitcnt vmcnt(6)
	v_cvt_f32_f16_e32 v54, v54
	v_cvt_f32_ubyte0_e32 v85, v28
	v_cvt_f32_ubyte1_e32 v86, v28
	v_cvt_f32_ubyte2_e32 v87, v28
	v_cvt_f32_ubyte3_e32 v88, v28
	v_fmac_f32_e32 v2, v85, v54
	v_fmac_f32_e32 v3, v86, v54
	v_fmac_f32_e32 v4, v87, v54
	v_fmac_f32_e32 v5, v88, v54
	v_cvt_f32_ubyte0_e32 v85, v29
	v_cvt_f32_ubyte1_e32 v86, v29
	v_cvt_f32_ubyte2_e32 v87, v29
	v_cvt_f32_ubyte3_e32 v88, v29
	v_fmac_f32_e32 v6, v85, v54
	v_fmac_f32_e32 v7, v86, v54
	v_fmac_f32_e32 v8, v87, v54
	v_fmac_f32_e32 v9, v88, v54
	v_cvt_f32_ubyte0_e32 v85, v30
	v_cvt_f32_ubyte1_e32 v86, v30
	v_cvt_f32_ubyte2_e32 v87, v30
	v_cvt_f32_ubyte3_e32 v88, v30
	v_fmac_f32_e32 v10, v85, v54
	v_fmac_f32_e32 v11, v86, v54
	v_fmac_f32_e32 v12, v87, v54
	v_fmac_f32_e32 v13, v88, v54
	v_cvt_f32_ubyte0_e32 v85, v31
	v_cvt_f32_ubyte1_e32 v86, v31
	v_cvt_f32_ubyte2_e32 v87, v31
	v_cvt_f32_ubyte3_e32 v88, v31
	v_fmac_f32_e32 v14, v85, v54
	v_fmac_f32_e32 v15, v86, v54
	v_fmac_f32_e32 v16, v87, v54
	v_fmac_f32_e32 v17, v88, v54
	v_and_b32_e32 v84, 0xffff, v80
	v_lshl_or_b32 v83, v84, 7, v89
	v_cmp_lt_i32_e32 vcc, 26, v78
	s_mov_b64 exec, vcc
	global_load_dwordx4 v[28:31], v83, s[12:13]
	s_mov_b64 exec, -1
	v_lshlrev_b32_e32 v109, 1, v84
	global_load_ushort v54, v109, s[14:15]
	s_waitcnt vmcnt(6)
	v_cvt_f32_f16_e32 v55, v55
	v_cvt_f32_ubyte0_e32 v85, v32
	v_cvt_f32_ubyte1_e32 v86, v32
	v_cvt_f32_ubyte2_e32 v87, v32
	v_cvt_f32_ubyte3_e32 v88, v32
	v_fmac_f32_e32 v2, v85, v55
	v_fmac_f32_e32 v3, v86, v55
	v_fmac_f32_e32 v4, v87, v55
	v_fmac_f32_e32 v5, v88, v55
	v_cvt_f32_ubyte0_e32 v85, v33
	v_cvt_f32_ubyte1_e32 v86, v33
	v_cvt_f32_ubyte2_e32 v87, v33
	v_cvt_f32_ubyte3_e32 v88, v33
	v_fmac_f32_e32 v6, v85, v55
	v_fmac_f32_e32 v7, v86, v55
	v_fmac_f32_e32 v8, v87, v55
	v_fmac_f32_e32 v9, v88, v55
	v_cvt_f32_ubyte0_e32 v85, v34
	v_cvt_f32_ubyte1_e32 v86, v34
	v_cvt_f32_ubyte2_e32 v87, v34
	v_cvt_f32_ubyte3_e32 v88, v34
	v_fmac_f32_e32 v10, v85, v55
	v_fmac_f32_e32 v11, v86, v55
	v_fmac_f32_e32 v12, v87, v55
	v_fmac_f32_e32 v13, v88, v55
	v_cvt_f32_ubyte0_e32 v85, v35
	v_cvt_f32_ubyte1_e32 v86, v35
	v_cvt_f32_ubyte2_e32 v87, v35
	v_cvt_f32_ubyte3_e32 v88, v35
	v_fmac_f32_e32 v14, v85, v55
	v_fmac_f32_e32 v15, v86, v55
	v_fmac_f32_e32 v16, v87, v55
	v_fmac_f32_e32 v17, v88, v55
	v_lshrrev_b32_e32 v84, 16, v80
	v_lshl_or_b32 v83, v84, 7, v89
	v_cmp_lt_i32_e32 vcc, 27, v78
	s_mov_b64 exec, vcc
	global_load_dwordx4 v[32:35], v83, s[12:13]
	s_mov_b64 exec, -1
	v_lshlrev_b32_e32 v109, 1, v84
	global_load_ushort v55, v109, s[14:15]
	s_cmp_le_u32 s40, 28
	s_cbranch_scc1 .Lg2_tail0
	s_waitcnt lgkmcnt(0)
	ds_bpermute_b32 v80, v90, v74 offset:28
	s_waitcnt vmcnt(6)
	v_cvt_f32_f16_e32 v52, v52
	v_cvt_f32_ubyte0_e32 v85, v20
	v_cvt_f32_ubyte1_e32 v86, v20
	v_cvt_f32_ubyte2_e32 v87, v20
	v_cvt_f32_ubyte3_e32 v88, v20
	v_fmac_f32_e32 v2, v85, v52
	v_fmac_f32_e32 v3, v86, v52
	v_fmac_f32_e32 v4, v87, v52
	v_fmac_f32_e32 v5, v88, v52
	v_cvt_f32_ubyte0_e32 v85, v21
	v_cvt_f32_ubyte1_e32 v86, v21
	v_cvt_f32_ubyte2_e32 v87, v21
	v_cvt_f32_ubyte3_e32 v88, v21
	v_fmac_f32_e32 v6, v85, v52
	v_fmac_f32_e32 v7, v86, v52
	v_fmac_f32_e32 v8, v87, v52
	v_fmac_f32_e32 v9, v88, v52
	v_cvt_f32_ubyte0_e32 v85, v22
	v_cvt_f32_ubyte1_e32 v86, v22
	v_cvt_f32_ubyte2_e32 v87, v22
	v_cvt_f32_ubyte3_e32 v88, v22
	v_fmac_f32_e32 v10, v85, v52
	v_fmac_f32_e32 v11, v86, v52
	v_fmac_f32_e32 v12, v87, v52
	v_fmac_f32_e32 v13, v88, v52
	v_cvt_f32_ubyte0_e32 v85, v23
	v_cvt_f32_ubyte1_e32 v86, v23
	v_cvt_f32_ubyte2_e32 v87, v23
	v_cvt_f32_ubyte3_e32 v88, v23
	v_fmac_f32_e32 v14, v85, v52
	v_fmac_f32_e32 v15, v86, v52
	v_fmac_f32_e32 v16, v87, v52
	v_fmac_f32_e32 v17, v88, v52
	v_and_b32_e32 v84, 0xffff, v79
	v_lshl_or_b32 v83, v84, 7, v89
	v_cmp_lt_i32_e32 vcc, 28, v78
	s_mov_b64 exec, vcc
	global_load_dwordx4 v[20:23], v83, s[12:13]
	s_mov_b64 exec, -1
	v_lshlrev_b32_e32 v109, 1, v84
	global_load_ushort v52, v109, s[14:15]
	s_waitcnt vmcnt(6)
	v_cvt_f32_f16_e32 v53, v53
	v_cvt_f32_ubyte0_e32 v85, v24
	v_cvt_f32_ubyte1_e32 v86, v24
	v_cvt_f32_ubyte2_e32 v87, v24
	v_cvt_f32_ubyte3_e32 v88, v24
	v_fmac_f32_e32 v2, v85, v53
	v_fmac_f32_e32 v3, v86, v53
	v_fmac_f32_e32 v4, v87, v53
	v_fmac_f32_e32 v5, v88, v53
	v_cvt_f32_ubyte0_e32 v85, v25
	v_cvt_f32_ubyte1_e32 v86, v25
	v_cvt_f32_ubyte2_e32 v87, v25
	v_cvt_f32_ubyte3_e32 v88, v25
	v_fmac_f32_e32 v6, v85, v53
	v_fmac_f32_e32 v7, v86, v53
	v_fmac_f32_e32 v8, v87, v53
	v_fmac_f32_e32 v9, v88, v53
	v_cvt_f32_ubyte0_e32 v85, v26
	v_cvt_f32_ubyte1_e32 v86, v26
	v_cvt_f32_ubyte2_e32 v87, v26
	v_cvt_f32_ubyte3_e32 v88, v26
	v_fmac_f32_e32 v10, v85, v53
	v_fmac_f32_e32 v11, v86, v53
	v_fmac_f32_e32 v12, v87, v53
	v_fmac_f32_e32 v13, v88, v53
	v_cvt_f32_ubyte0_e32 v85, v27
	v_cvt_f32_ubyte1_e32 v86, v27
	v_cvt_f32_ubyte2_e32 v87, v27
	v_cvt_f32_ubyte3_e32 v88, v27
	v_fmac_f32_e32 v14, v85, v53
	v_fmac_f32_e32 v15, v86, v53
	v_fmac_f32_e32 v16, v87, v53
	v_fmac_f32_e32 v17, v88, v53
	v_lshrrev_b32_e32 v84, 16, v79
	v_lshl_or_b32 v83, v84, 7, v89
	v_cmp_lt_i32_e32 vcc, 29, v78
	s_mov_b64 exec, vcc
	global_load_dwordx4 v[24:27], v83, s[12:13]
	s_mov_b64 exec, -1
	v_lshlrev_b32_e32 v109, 1, v84
	global_load_ushort v53, v109, s[14:15]
	s_waitcnt lgkmcnt(0)
	s_waitcnt vmcnt(6)
	v_cvt_f32_f16_e32 v54, v54
	v_cvt_f32_ubyte0_e32 v85, v28
	v_cvt_f32_ubyte1_e32 v86, v28
	v_cvt_f32_ubyte2_e32 v87, v28
	v_cvt_f32_ubyte3_e32 v88, v28
	v_fmac_f32_e32 v2, v85, v54
	v_fmac_f32_e32 v3, v86, v54
	v_fmac_f32_e32 v4, v87, v54
	v_fmac_f32_e32 v5, v88, v54
	v_cvt_f32_ubyte0_e32 v85, v29
	v_cvt_f32_ubyte1_e32 v86, v29
	v_cvt_f32_ubyte2_e32 v87, v29
	v_cvt_f32_ubyte3_e32 v88, v29
	v_fmac_f32_e32 v6, v85, v54
	v_fmac_f32_e32 v7, v86, v54
	v_fmac_f32_e32 v8, v87, v54
	v_fmac_f32_e32 v9, v88, v54
	v_cvt_f32_ubyte0_e32 v85, v30
	v_cvt_f32_ubyte1_e32 v86, v30
	v_cvt_f32_ubyte2_e32 v87, v30
	v_cvt_f32_ubyte3_e32 v88, v30
	v_fmac_f32_e32 v10, v85, v54
	v_fmac_f32_e32 v11, v86, v54
	v_fmac_f32_e32 v12, v87, v54
	v_fmac_f32_e32 v13, v88, v54
	v_cvt_f32_ubyte0_e32 v85, v31
	v_cvt_f32_ubyte1_e32 v86, v31
	v_cvt_f32_ubyte2_e32 v87, v31
	v_cvt_f32_ubyte3_e32 v88, v31
	v_fmac_f32_e32 v14, v85, v54
	v_fmac_f32_e32 v15, v86, v54
	v_fmac_f32_e32 v16, v87, v54
	v_fmac_f32_e32 v17, v88, v54
	v_and_b32_e32 v84, 0xffff, v80
	v_lshl_or_b32 v83, v84, 7, v89
	v_cmp_lt_i32_e32 vcc, 30, v78
	s_mov_b64 exec, vcc
	global_load_dwordx4 v[28:31], v83, s[12:13]
	s_mov_b64 exec, -1
	v_lshlrev_b32_e32 v109, 1, v84
	global_load_ushort v54, v109, s[14:15]
	s_waitcnt vmcnt(6)
	v_cvt_f32_f16_e32 v55, v55
	v_cvt_f32_ubyte0_e32 v85, v32
	v_cvt_f32_ubyte1_e32 v86, v32
	v_cvt_f32_ubyte2_e32 v87, v32
	v_cvt_f32_ubyte3_e32 v88, v32
	v_fmac_f32_e32 v2, v85, v55
	v_fmac_f32_e32 v3, v86, v55
	v_fmac_f32_e32 v4, v87, v55
	v_fmac_f32_e32 v5, v88, v55
	v_cvt_f32_ubyte0_e32 v85, v33
	v_cvt_f32_ubyte1_e32 v86, v33
	v_cvt_f32_ubyte2_e32 v87, v33
	v_cvt_f32_ubyte3_e32 v88, v33
	v_fmac_f32_e32 v6, v85, v55
	v_fmac_f32_e32 v7, v86, v55
	v_fmac_f32_e32 v8, v87, v55
	v_fmac_f32_e32 v9, v88, v55
	v_cvt_f32_ubyte0_e32 v85, v34
	v_cvt_f32_ubyte1_e32 v86, v34
	v_cvt_f32_ubyte2_e32 v87, v34
	v_cvt_f32_ubyte3_e32 v88, v34
	v_fmac_f32_e32 v10, v85, v55
	v_fmac_f32_e32 v11, v86, v55
	v_fmac_f32_e32 v12, v87, v55
	v_fmac_f32_e32 v13, v88, v55
	v_cvt_f32_ubyte0_e32 v85, v35
	v_cvt_f32_ubyte1_e32 v86, v35
	v_cvt_f32_ubyte2_e32 v87, v35
	v_cvt_f32_ubyte3_e32 v88, v35
	v_fmac_f32_e32 v14, v85, v55
	v_fmac_f32_e32 v15, v86, v55
	v_fmac_f32_e32 v16, v87, v55
	v_fmac_f32_e32 v17, v88, v55
	v_lshrrev_b32_e32 v84, 16, v80
	v_lshl_or_b32 v83, v84, 7, v89
	v_cmp_lt_i32_e32 vcc, 31, v78
	s_mov_b64 exec, vcc
	global_load_dwordx4 v[32:35], v83, s[12:13]
	s_mov_b64 exec, -1
	v_lshlrev_b32_e32 v109, 1, v84
	global_load_ushort v55, v109, s[14:15]
